# P6: gate loads of the mid hook issued one quarter ahead (alternating register sets), epilogue second-half gate loads issued with the first; P2/P6/P10 epilogue-start loads issued before the half-alignm
# speedup vs baseline: 1.0043x; 1.0043x over previous
.LBB0_326:
	v_add_u32_e32 v44, 0x10000, v162
	v_add_u32_e32 v168, 0x14000, v162
	ds_read_b128 v[24:27], v44
	ds_read_b128 v[28:31], v44 offset:1024
	ds_read_b128 v[40:43], v44 offset:2048
	ds_read_b128 v[44:47], v44 offset:3072
	ds_read_b128 v[146:149], v168
	ds_read_b128 v[150:153], v168 offset:1024
	ds_read_b128 v[164:167], v168 offset:2048
	ds_read_b128 v[168:171], v168 offset:3072
	s_cmp_eq_u32 s6, 28
	s_cselect_b32 s7, s54, s5
	s_cselect_b32 s8, s55, s4
	s_add_i32 s9, s5, 0xffffff80
	s_mov_b32 m0, s49
	ds_read_b128 v[172:175], v163
	ds_read_b128 v[176:179], v163 offset:1024
	ds_read_b128 v[180:183], v163 offset:2048
	ds_read_b128 v[184:187], v163 offset:3072
	ds_read_b128 v[188:191], v163 offset:4096
	ds_read_b128 v[192:195], v163 offset:5120
	ds_read_b128 v[196:199], v163 offset:6144
	ds_read_b128 v[200:203], v163 offset:7168
	buffer_load_dwordx4 v158, s[12:15], s9 offen lds
	s_mov_b32 m0, s50
	s_nop 0
	buffer_load_dwordx4 v159, s[12:15], s9 offen lds
	s_waitcnt vmcnt(8)
	s_waitcnt lgkmcnt(0)
	s_barrier
	s_setprio 1
	s_waitcnt lgkmcnt(7)
	v_mfma_f32_16x16x32_bf16 v[136:139], v[24:27], v[172:175], v[136:139]
	v_mfma_f32_16x16x32_bf16 v[140:143], v[40:43], v[172:175], v[140:143]
	s_waitcnt lgkmcnt(5)
	v_mfma_f32_16x16x32_bf16 v[124:127], v[24:27], v[180:183], v[124:127]
	v_mfma_f32_16x16x32_bf16 v[120:123], v[40:43], v[180:183], v[120:123]
	s_waitcnt lgkmcnt(3)
	v_mfma_f32_16x16x32_bf16 v[108:111], v[24:27], v[188:191], v[108:111]
	v_mfma_f32_16x16x32_bf16 v[104:107], v[40:43], v[188:191], v[104:107]
	s_waitcnt lgkmcnt(1)
	v_mfma_f32_16x16x32_bf16 v[92:95], v[24:27], v[196:199], v[92:95]
	v_mfma_f32_16x16x32_bf16 v[88:91], v[40:43], v[196:199], v[88:91]
	v_mfma_f32_16x16x32_bf16 v[136:139], v[28:31], v[176:179], v[136:139]
	v_mfma_f32_16x16x32_bf16 v[140:143], v[44:47], v[176:179], v[140:143]
	v_mfma_f32_16x16x32_bf16 v[124:127], v[28:31], v[184:187], v[124:127]
	v_mfma_f32_16x16x32_bf16 v[120:123], v[44:47], v[184:187], v[120:123]
	v_mfma_f32_16x16x32_bf16 v[108:111], v[28:31], v[192:195], v[108:111]
	v_mfma_f32_16x16x32_bf16 v[104:107], v[44:47], v[192:195], v[104:107]
	s_waitcnt lgkmcnt(0)
	v_mfma_f32_16x16x32_bf16 v[92:95], v[28:31], v[200:203], v[92:95]
	v_mfma_f32_16x16x32_bf16 v[88:91], v[44:47], v[200:203], v[88:91]
	s_setprio 0
	s_setprio 1
	v_mfma_f32_16x16x32_bf16 v[132:135], v[146:149], v[172:175], v[132:135]
	v_mfma_f32_16x16x32_bf16 v[128:131], v[164:167], v[172:175], v[128:131]
	v_mfma_f32_16x16x32_bf16 v[116:119], v[146:149], v[180:183], v[116:119]
	v_mfma_f32_16x16x32_bf16 v[112:115], v[164:167], v[180:183], v[112:115]
	v_mfma_f32_16x16x32_bf16 v[100:103], v[146:149], v[188:191], v[100:103]
	v_mfma_f32_16x16x32_bf16 v[96:99], v[164:167], v[188:191], v[96:99]
	v_mfma_f32_16x16x32_bf16 v[84:87], v[146:149], v[196:199], v[84:87]
	v_mfma_f32_16x16x32_bf16 v[80:83], v[164:167], v[196:199], v[80:83]
	v_mfma_f32_16x16x32_bf16 v[132:135], v[150:153], v[176:179], v[132:135]
	v_mfma_f32_16x16x32_bf16 v[128:131], v[168:171], v[176:179], v[128:131]
	v_mfma_f32_16x16x32_bf16 v[116:119], v[150:153], v[184:187], v[116:119]
	v_mfma_f32_16x16x32_bf16 v[112:115], v[168:171], v[184:187], v[112:115]
	v_mfma_f32_16x16x32_bf16 v[100:103], v[150:153], v[192:195], v[100:103]
	v_mfma_f32_16x16x32_bf16 v[96:99], v[168:171], v[192:195], v[96:99]
	v_mfma_f32_16x16x32_bf16 v[84:87], v[150:153], v[200:203], v[84:87]
	v_mfma_f32_16x16x32_bf16 v[80:83], v[168:171], v[200:203], v[80:83]
	s_setprio 0
	s_barrier
	s_mov_b32 m0, s35
	s_mov_b32 s18, s14
	s_mov_b32 s19, s15
	ds_read_b128 v[172:175], v163 offset:16384
	ds_read_b128 v[176:179], v163 offset:17408
	ds_read_b128 v[180:183], v163 offset:18432
	ds_read_b128 v[184:187], v163 offset:19456
	ds_read_b128 v[188:191], v163 offset:20480
	ds_read_b128 v[192:195], v163 offset:21504
	ds_read_b128 v[196:199], v163 offset:22528
	ds_read_b128 v[200:203], v163 offset:23552
	buffer_load_dwordx4 v154, s[16:19], s8 offen lds
	s_mov_b32 m0, s36
	s_add_i32 s9, s8, 0x80000
	buffer_load_dwordx4 v155, s[16:19], s8 offen lds
	s_mov_b32 m0, s37
	s_nop 0
	buffer_load_dwordx4 v154, s[16:19], s9 offen lds
	s_mov_b32 m0, s38
	s_nop 0
	buffer_load_dwordx4 v155, s[16:19], s9 offen lds
	s_mov_b32 m0, s34
	s_nop 0
	buffer_load_dwordx4 v156, s[12:15], s7 offen lds
	s_mov_b32 m0, s39
	s_nop 0
	buffer_load_dwordx4 v157, s[12:15], s7 offen lds
	s_waitcnt vmcnt(8)
	s_waitcnt lgkmcnt(0)
	s_barrier
	s_setprio 1
	s_waitcnt lgkmcnt(7)
	v_mfma_f32_16x16x32_bf16 v[76:79], v[24:27], v[172:175], v[76:79]
	v_mfma_f32_16x16x32_bf16 v[72:75], v[40:43], v[172:175], v[72:75]
	s_waitcnt lgkmcnt(5)
	v_mfma_f32_16x16x32_bf16 v[60:63], v[24:27], v[180:183], v[60:63]
	v_mfma_f32_16x16x32_bf16 v[56:59], v[40:43], v[180:183], v[56:59]
	s_waitcnt lgkmcnt(3)
	v_mfma_f32_16x16x32_bf16 v[36:39], v[24:27], v[188:191], v[36:39]
	v_mfma_f32_16x16x32_bf16 v[32:35], v[40:43], v[188:191], v[32:35]
	s_waitcnt lgkmcnt(1)
	v_mfma_f32_16x16x32_bf16 v[12:15], v[24:27], v[196:199], v[12:15]
	v_mfma_f32_16x16x32_bf16 v[8:11], v[40:43], v[196:199], v[8:11]
	v_mfma_f32_16x16x32_bf16 v[76:79], v[28:31], v[176:179], v[76:79]
	v_mfma_f32_16x16x32_bf16 v[72:75], v[44:47], v[176:179], v[72:75]
	v_mfma_f32_16x16x32_bf16 v[60:63], v[28:31], v[184:187], v[60:63]
	v_mfma_f32_16x16x32_bf16 v[56:59], v[44:47], v[184:187], v[56:59]
	v_mfma_f32_16x16x32_bf16 v[36:39], v[28:31], v[192:195], v[36:39]
	v_mfma_f32_16x16x32_bf16 v[32:35], v[44:47], v[192:195], v[32:35]
	s_waitcnt lgkmcnt(0)
	v_mfma_f32_16x16x32_bf16 v[12:15], v[28:31], v[200:203], v[12:15]
	v_mfma_f32_16x16x32_bf16 v[8:11], v[44:47], v[200:203], v[8:11]
	s_setprio 0
	s_setprio 1
	v_mfma_f32_16x16x32_bf16 v[20:23], v[146:149], v[188:191], v[20:23]
	v_mfma_f32_16x16x32_bf16 v[16:19], v[164:167], v[188:191], v[16:19]
	v_mfma_f32_16x16x32_bf16 v[4:7], v[146:149], v[196:199], v[4:7]
	v_mfma_f32_16x16x32_bf16 v[0:3], v[164:167], v[196:199], v[0:3]
	v_mfma_f32_16x16x32_bf16 v[24:27], v[146:149], v[172:175], v[68:71]
	v_mfma_f32_16x16x32_bf16 v[28:31], v[164:167], v[172:175], v[64:67]
	v_mfma_f32_16x16x32_bf16 v[40:43], v[146:149], v[180:183], v[52:55]
	v_mfma_f32_16x16x32_bf16 v[44:47], v[164:167], v[180:183], v[48:51]
	v_mfma_f32_16x16x32_bf16 v[20:23], v[150:153], v[192:195], v[20:23]
	v_mfma_f32_16x16x32_bf16 v[16:19], v[168:171], v[192:195], v[16:19]
	v_mfma_f32_16x16x32_bf16 v[4:7], v[150:153], v[200:203], v[4:7]
	v_mfma_f32_16x16x32_bf16 v[0:3], v[168:171], v[200:203], v[0:3]
	v_mfma_f32_16x16x32_bf16 v[24:27], v[150:153], v[176:179], v[24:27]
	v_mfma_f32_16x16x32_bf16 v[28:31], v[168:171], v[176:179], v[28:31]
	v_mfma_f32_16x16x32_bf16 v[40:43], v[150:153], v[184:187], v[40:43]
	v_mfma_f32_16x16x32_bf16 v[44:47], v[168:171], v[184:187], v[44:47]
	s_setprio 0
	s_barrier
	v_add_u32_e32 v68, 0x18000, v162
	v_add_u32_e32 v168, 0x1c000, v162
	ds_read_b128 v[48:51], v68
	ds_read_b128 v[52:55], v68 offset:1024
	ds_read_b128 v[64:67], v68 offset:2048
	ds_read_b128 v[68:71], v68 offset:3072
	ds_read_b128 v[146:149], v168
	ds_read_b128 v[150:153], v168 offset:1024
	ds_read_b128 v[164:167], v168 offset:2048
	ds_read_b128 v[168:171], v168 offset:3072
	s_mov_b32 m0, s40
	ds_read_b128 v[172:175], v163 offset:32768
	ds_read_b128 v[176:179], v163 offset:33792
	ds_read_b128 v[180:183], v163 offset:34816
	ds_read_b128 v[184:187], v163 offset:35840
	ds_read_b128 v[188:191], v163 offset:36864
	ds_read_b128 v[192:195], v163 offset:37888
	ds_read_b128 v[196:199], v163 offset:38912
	ds_read_b128 v[200:203], v163 offset:39936
	buffer_load_dwordx4 v158, s[12:15], s7 offen lds
	s_mov_b32 m0, s41
	s_nop 0
	buffer_load_dwordx4 v159, s[12:15], s7 offen lds
	s_waitcnt vmcnt(8)
	s_waitcnt lgkmcnt(0)
	s_barrier
	s_setprio 1
	s_waitcnt lgkmcnt(7)
	v_mfma_f32_16x16x32_bf16 v[136:139], v[48:51], v[172:175], v[136:139]
	v_mfma_f32_16x16x32_bf16 v[140:143], v[64:67], v[172:175], v[140:143]
	s_waitcnt lgkmcnt(5)
	v_mfma_f32_16x16x32_bf16 v[124:127], v[48:51], v[180:183], v[124:127]
	v_mfma_f32_16x16x32_bf16 v[120:123], v[64:67], v[180:183], v[120:123]
	s_waitcnt lgkmcnt(3)
	v_mfma_f32_16x16x32_bf16 v[108:111], v[48:51], v[188:191], v[108:111]
	v_mfma_f32_16x16x32_bf16 v[104:107], v[64:67], v[188:191], v[104:107]
	s_waitcnt lgkmcnt(1)
	v_mfma_f32_16x16x32_bf16 v[92:95], v[48:51], v[196:199], v[92:95]
	v_mfma_f32_16x16x32_bf16 v[88:91], v[64:67], v[196:199], v[88:91]
	v_mfma_f32_16x16x32_bf16 v[136:139], v[52:55], v[176:179], v[136:139]
	v_mfma_f32_16x16x32_bf16 v[140:143], v[68:71], v[176:179], v[140:143]
	v_mfma_f32_16x16x32_bf16 v[124:127], v[52:55], v[184:187], v[124:127]
	v_mfma_f32_16x16x32_bf16 v[120:123], v[68:71], v[184:187], v[120:123]
	v_mfma_f32_16x16x32_bf16 v[108:111], v[52:55], v[192:195], v[108:111]
	v_mfma_f32_16x16x32_bf16 v[104:107], v[68:71], v[192:195], v[104:107]
	s_waitcnt lgkmcnt(0)
	v_mfma_f32_16x16x32_bf16 v[92:95], v[52:55], v[200:203], v[92:95]
	v_mfma_f32_16x16x32_bf16 v[88:91], v[68:71], v[200:203], v[88:91]
	s_setprio 0
	s_setprio 1
	v_mfma_f32_16x16x32_bf16 v[132:135], v[146:149], v[172:175], v[132:135]
	v_mfma_f32_16x16x32_bf16 v[128:131], v[164:167], v[172:175], v[128:131]
	v_mfma_f32_16x16x32_bf16 v[116:119], v[146:149], v[180:183], v[116:119]
	v_mfma_f32_16x16x32_bf16 v[112:115], v[164:167], v[180:183], v[112:115]
	v_mfma_f32_16x16x32_bf16 v[100:103], v[146:149], v[188:191], v[100:103]
	v_mfma_f32_16x16x32_bf16 v[96:99], v[164:167], v[188:191], v[96:99]
	v_mfma_f32_16x16x32_bf16 v[84:87], v[146:149], v[196:199], v[84:87]
	v_mfma_f32_16x16x32_bf16 v[80:83], v[164:167], v[196:199], v[80:83]
	v_mfma_f32_16x16x32_bf16 v[132:135], v[150:153], v[176:179], v[132:135]
	v_mfma_f32_16x16x32_bf16 v[128:131], v[168:171], v[176:179], v[128:131]
	v_mfma_f32_16x16x32_bf16 v[116:119], v[150:153], v[184:187], v[116:119]
	v_mfma_f32_16x16x32_bf16 v[112:115], v[168:171], v[184:187], v[112:115]
	v_mfma_f32_16x16x32_bf16 v[100:103], v[150:153], v[192:195], v[100:103]
	v_mfma_f32_16x16x32_bf16 v[96:99], v[168:171], v[192:195], v[96:99]
	v_mfma_f32_16x16x32_bf16 v[84:87], v[150:153], v[200:203], v[84:87]
	v_mfma_f32_16x16x32_bf16 v[80:83], v[168:171], v[200:203], v[80:83]
	s_setprio 0
	s_barrier
	s_mov_b32 m0, s43
	s_or_b32 s9, s8, 0x80
	ds_read_b128 v[172:175], v163 offset:49152
	ds_read_b128 v[176:179], v163 offset:50176
	ds_read_b128 v[180:183], v163 offset:51200
	ds_read_b128 v[184:187], v163 offset:52224
	ds_read_b128 v[188:191], v163 offset:53248
	ds_read_b128 v[192:195], v163 offset:54272
	ds_read_b128 v[196:199], v163 offset:55296
	ds_read_b128 v[200:203], v163 offset:56320
	buffer_load_dwordx4 v154, s[16:19], s9 offen lds
	s_mov_b32 m0, s44
	s_add_i32 s8, s8, 0x80080
	buffer_load_dwordx4 v155, s[16:19], s9 offen lds
	s_mov_b32 m0, s47
	s_bitset1_b32 s7, 7
	buffer_load_dwordx4 v154, s[16:19], s8 offen lds
	s_mov_b32 m0, s48
	s_nop 0
	buffer_load_dwordx4 v155, s[16:19], s8 offen lds
	s_mov_b32 m0, s45
	s_nop 0
	buffer_load_dwordx4 v156, s[12:15], s7 offen lds
	s_mov_b32 m0, s46
	s_nop 0
	buffer_load_dwordx4 v157, s[12:15], s7 offen lds
	s_waitcnt vmcnt(8)
	s_waitcnt lgkmcnt(0)
	s_barrier
	s_setprio 1
	s_waitcnt lgkmcnt(7)
	v_mfma_f32_16x16x32_bf16 v[76:79], v[48:51], v[172:175], v[76:79]
	v_mfma_f32_16x16x32_bf16 v[72:75], v[64:67], v[172:175], v[72:75]
	s_waitcnt lgkmcnt(5)
	v_mfma_f32_16x16x32_bf16 v[60:63], v[48:51], v[180:183], v[60:63]
	v_mfma_f32_16x16x32_bf16 v[56:59], v[64:67], v[180:183], v[56:59]
	s_waitcnt lgkmcnt(3)
	v_mfma_f32_16x16x32_bf16 v[36:39], v[48:51], v[188:191], v[36:39]
	v_mfma_f32_16x16x32_bf16 v[32:35], v[64:67], v[188:191], v[32:35]
	s_waitcnt lgkmcnt(1)
	v_mfma_f32_16x16x32_bf16 v[12:15], v[48:51], v[196:199], v[12:15]
	v_mfma_f32_16x16x32_bf16 v[8:11], v[64:67], v[196:199], v[8:11]
	v_mfma_f32_16x16x32_bf16 v[76:79], v[52:55], v[176:179], v[76:79]
	v_mfma_f32_16x16x32_bf16 v[72:75], v[68:71], v[176:179], v[72:75]
	v_mfma_f32_16x16x32_bf16 v[60:63], v[52:55], v[184:187], v[60:63]
	v_mfma_f32_16x16x32_bf16 v[56:59], v[68:71], v[184:187], v[56:59]
	v_mfma_f32_16x16x32_bf16 v[36:39], v[52:55], v[192:195], v[36:39]
	v_mfma_f32_16x16x32_bf16 v[32:35], v[68:71], v[192:195], v[32:35]
	s_waitcnt lgkmcnt(0)
	v_mfma_f32_16x16x32_bf16 v[12:15], v[52:55], v[200:203], v[12:15]
	v_mfma_f32_16x16x32_bf16 v[8:11], v[68:71], v[200:203], v[8:11]
	s_setprio 0
	s_setprio 1
	v_mfma_f32_16x16x32_bf16 v[24:27], v[146:149], v[172:175], v[24:27]
	v_mfma_f32_16x16x32_bf16 v[68:71], v[150:153], v[176:179], v[24:27]
	v_mfma_f32_16x16x32_bf16 v[24:27], v[164:167], v[172:175], v[28:31]
	v_mfma_f32_16x16x32_bf16 v[64:67], v[168:171], v[176:179], v[24:27]
	v_mfma_f32_16x16x32_bf16 v[24:27], v[146:149], v[180:183], v[40:43]
	v_mfma_f32_16x16x32_bf16 v[52:55], v[150:153], v[184:187], v[24:27]
	v_mfma_f32_16x16x32_bf16 v[24:27], v[164:167], v[180:183], v[44:47]
	v_mfma_f32_16x16x32_bf16 v[20:23], v[146:149], v[188:191], v[20:23]
	v_mfma_f32_16x16x32_bf16 v[16:19], v[164:167], v[188:191], v[16:19]
	v_mfma_f32_16x16x32_bf16 v[4:7], v[146:149], v[196:199], v[4:7]
	v_mfma_f32_16x16x32_bf16 v[0:3], v[164:167], v[196:199], v[0:3]
	v_mfma_f32_16x16x32_bf16 v[48:51], v[168:171], v[184:187], v[24:27]
	v_mfma_f32_16x16x32_bf16 v[20:23], v[150:153], v[192:195], v[20:23]
	v_mfma_f32_16x16x32_bf16 v[16:19], v[168:171], v[192:195], v[16:19]
	v_mfma_f32_16x16x32_bf16 v[4:7], v[150:153], v[200:203], v[4:7]
	v_mfma_f32_16x16x32_bf16 v[0:3], v[168:171], v[200:203], v[0:3]
	s_setprio 0
	s_barrier
	s_add_i32 s6, s6, 2
	s_addk_i32 s4, 0x100
	s_addk_i32 s5, 0x100
	s_cmp_gt_u32 s6, 29
	s_cbranch_scc0 .LBB0_326
	v_lshl_or_b32 v146, s30, 8, v161
	v_ashrrev_i32_e32 v147, 31, v146
	v_lshl_add_u64 v[28:29], v[146:147], 2, s[22:23]
	global_load_dwordx4 v[40:43], v[28:29], off offset:16
	global_load_dwordx4 v[44:47], v[28:29], off
	global_load_dwordx4 v[24:27], v[28:29], off offset:528
	s_nop 0
	global_load_dwordx4 v[28:31], v[28:29], off offset:512
	s_cmp_gt_i32 s30, 4
	s_cbranch_scc1 .Lp2_rope_pre_done
	s_and_saveexec_b64 vcc, s[26:27]
	v_lshl_add_u32 v244, s33, 8, v160
	v_add_u32_e32 v246, 0x80, v244
	v_ashrrev_i32_e32 v245, 31, v244
	v_ashrrev_i32_e32 v247, 31, v246
	v_lshlrev_b64 v[244:245], 6, v[244:245]
	v_lshlrev_b64 v[246:247], 6, v[246:247]
	v_lshl_add_u64 v[244:245], v[144:145], 0, v[244:245]
	v_lshl_add_u64 v[246:247], v[144:145], 0, v[246:247]
	global_load_dwordx4 v[176:179], v[244:245], off
	global_load_dwordx4 v[180:183], v[244:245], off offset:16
	global_load_dwordx4 v[184:187], v[244:245], off offset:1024
	global_load_dwordx4 v[188:191], v[244:245], off offset:1040
	global_load_dwordx4 v[192:195], v[244:245], off offset:2048
	global_load_dwordx4 v[196:199], v[244:245], off offset:2064
	global_load_dwordx4 v[204:207], v[244:245], off offset:3072
	global_load_dwordx4 v[208:211], v[244:245], off offset:3088
	global_load_dwordx4 v[212:215], v[246:247], off
	global_load_dwordx4 v[216:219], v[246:247], off offset:16
	global_load_dwordx4 v[220:223], v[246:247], off offset:1024
	global_load_dwordx4 v[224:227], v[246:247], off offset:1040
	global_load_dwordx4 v[228:231], v[246:247], off offset:2048
	global_load_dwordx4 v[232:235], v[246:247], off offset:2064
	global_load_dwordx4 v[236:239], v[246:247], off offset:3072
	global_load_dwordx4 v[240:243], v[246:247], off offset:3088
	s_mov_b64 exec, vcc
.Lp2_rope_pre_done:
	s_and_b64 vcc, exec, s[24:25]
	s_cbranch_vccz .LBB0_329
	s_barrier

.LBB0_870:
	global_load_dwordx4 v[204:207], v[178:179], off
	global_load_dwordx4 v[208:211], v[144:145], off
	global_load_dwordx4 v[212:215], v[178:179], off offset:256
	global_load_dwordx4 v[216:219], v[144:145], off offset:256
	global_load_dwordx4 v[140:143], v[180:181], off
	global_load_dwordx4 v[132:135], v[180:181], off offset:256
	global_load_dwordx4 v[136:139], v[146:147], off
	global_load_dwordx4 v[128:131], v[146:147], off offset:256
	global_load_dwordx4 v[232:235], v[182:183], off offset:256
	global_load_dwordx4 v[236:239], v[174:175], off offset:256
	global_load_dwordx4 v[240:243], v[184:185], off
	global_load_dwordx4 v[244:247], v[184:185], off offset:256
	global_load_dwordx4 v[248:251], v[176:177], off
	s_waitcnt vmcnt(12)
	v_lshlrev_b32_e32 v220, 16, v204
	v_and_b32_e32 v204, 0xffff0000, v204
	v_lshlrev_b32_e32 v221, 16, v205
	v_lshlrev_b32_e32 v222, 16, v206
	v_lshlrev_b32_e32 v223, 16, v207
	v_and_b32_e32 v226, 0xffff0000, v207
	s_waitcnt vmcnt(11)
	v_lshlrev_b32_e32 v207, 16, v208
	v_and_b32_e32 v208, 0xffff0000, v208
	v_lshlrev_b32_e32 v224, 16, v209
	v_and_b32_e32 v209, 0xffff0000, v209
	v_lshlrev_b32_e32 v225, 16, v210
	v_and_b32_e32 v210, 0xffff0000, v210
	v_and_b32_e32 v205, 0xffff0000, v205
	v_and_b32_e32 v206, 0xffff0000, v206
	v_mul_f32_e32 v204, 0xbfb8aa3b, v204
	v_mul_f32_e32 v208, 0xbfb8aa3b, v208
	v_mul_f32_e32 v221, 0xbfb8aa3b, v221
	v_mul_f32_e32 v224, 0xbfb8aa3b, v224
	v_mul_f32_e32 v209, 0xbfb8aa3b, v209
	v_mul_f32_e32 v222, 0xbfb8aa3b, v222
	v_mul_f32_e32 v225, 0xbfb8aa3b, v225
	v_mul_f32_e32 v210, 0xbfb8aa3b, v210
	v_mul_f32_e32 v205, 0xbfb8aa3b, v205
	v_mul_f32_e32 v206, 0xbfb8aa3b, v206
	v_exp_f32_e32 v204, v204
	v_exp_f32_e32 v208, v208
	v_exp_f32_e32 v221, v221
	v_exp_f32_e32 v224, v224
	v_exp_f32_e32 v209, v209
	v_exp_f32_e32 v222, v222
	v_exp_f32_e32 v225, v225
	v_exp_f32_e32 v210, v210
	v_exp_f32_e32 v205, v205
	v_exp_f32_e32 v206, v206
	v_mul_f32_e32 v220, 0xbfb8aa3b, v220
	v_mul_f32_e32 v207, 0xbfb8aa3b, v207
	v_mul_f32_e32 v223, 0xbfb8aa3b, v223
	v_exp_f32_e32 v220, v220
	v_exp_f32_e32 v207, v207
	v_exp_f32_e32 v223, v223
	v_add_f32_e32 v228, 1.0, v204
	v_add_f32_e32 v208, 1.0, v208
	v_add_f32_e32 v221, 1.0, v221
	v_add_f32_e32 v224, 1.0, v224
	v_add_f32_e32 v209, 1.0, v209
	v_add_f32_e32 v222, 1.0, v222
	v_add_f32_e32 v225, 1.0, v225
	v_add_f32_e32 v210, 1.0, v210
	v_lshlrev_b32_e32 v227, 16, v211
	v_add_f32_e32 v229, 1.0, v205
	v_add_f32_e32 v230, 1.0, v206
	v_rcp_f32_e32 v205, v228
	v_min_f32_e32 v228, 0x49800000, v208
	v_rcp_f32_e32 v206, v221
	v_min_f32_e32 v221, 0x49800000, v224
	v_min_f32_e32 v224, 0x49800000, v209
	v_rcp_f32_e32 v208, v222
	v_min_f32_e32 v222, 0x49800000, v225
	v_min_f32_e32 v225, 0x49800000, v210
	v_and_b32_e32 v211, 0xffff0000, v211
	v_mul_f32_e32 v227, 0xbfb8aa3b, v227
	v_mul_f32_e32 v211, 0xbfb8aa3b, v211
	v_exp_f32_e32 v227, v227
	v_add_f32_e32 v220, 1.0, v220
	v_add_f32_e32 v207, 1.0, v207
	v_add_f32_e32 v223, 1.0, v223
	v_exp_f32_e32 v211, v211
	v_rcp_f32_e32 v204, v220
	v_min_f32_e32 v220, 0x49800000, v207
	v_rcp_f32_e32 v207, v229
	v_rcp_f32_e32 v210, v223
	v_mov_b32_e32 v223, v228
	v_mov_b32_e32 v229, v222
	v_rcp_f32_e32 v209, v230
	v_mov_b32_e32 v228, v221
	v_mov_b32_e32 v221, v223
	v_mov_b32_e32 v223, v224
	v_mov_b32_e32 v224, v229
	v_add_f32_e32 v227, 1.0, v227
	v_min_f32_e32 v227, 0x49800000, v227
	v_mul_f32_e32 v226, 0xbfb8aa3b, v226
	v_add_f32_e32 v211, 1.0, v211
	v_mov_b32_e32 v222, v228
	v_exp_f32_e32 v228, v226
	v_min_f32_e32 v229, 0x49800000, v211
	v_pk_mul_f32 v[208:209], v[208:209], v[224:225]
	v_pk_mul_f32 v[120:121], v[120:121], v[208:209]
	s_waitcnt vmcnt(9)
	v_and_b32_e32 v208, 0xffff0000, v216
	v_mul_f32_e32 v208, 0xbfb8aa3b, v208
	v_mov_b32_e32 v226, v227
	v_add_f32_e32 v211, 1.0, v228
	v_mov_b32_e32 v227, v229
	v_exp_f32_e32 v208, v208
	v_rcp_f32_e32 v211, v211
	v_pk_mul_f32 v[204:205], v[204:205], v[220:221]
	v_pk_mul_f32 v[206:207], v[206:207], v[222:223]
	v_pk_mul_f32 v[124:125], v[124:125], v[204:205]
	v_lshlrev_b32_e32 v204, 16, v212
	v_and_b32_e32 v205, 0xffff0000, v212
	v_and_b32_e32 v212, 0xffff0000, v217
	v_mul_f32_e32 v212, 0xbfb8aa3b, v212
	v_pk_mul_f32 v[126:127], v[126:127], v[206:207]
	v_lshlrev_b32_e32 v207, 16, v213
	v_add_f32_e32 v208, 1.0, v208
	v_exp_f32_e32 v212, v212
	v_pk_mul_f32 v[210:211], v[210:211], v[226:227]
	v_min_f32_e32 v208, 0x49800000, v208
	v_mul_f32_e32 v207, 0xbfb8aa3b, v207
	v_pk_mul_f32 v[122:123], v[122:123], v[210:211]
	v_and_b32_e32 v209, 0xffff0000, v213
	v_lshlrev_b32_e32 v211, 16, v214
	v_and_b32_e32 v213, 0xffff0000, v214
	v_lshlrev_b32_e32 v220, 16, v215
	v_and_b32_e32 v221, 0xffff0000, v215
	v_lshlrev_b32_e32 v214, 16, v218
	v_and_b32_e32 v215, 0xffff0000, v218
	v_exp_f32_e32 v218, v207
	v_lshlrev_b32_e32 v210, 16, v217
	v_add_f32_e32 v212, 1.0, v212
	v_mul_f32_e32 v214, 0xbfb8aa3b, v214
	v_lshlrev_b32_e32 v206, 16, v216
	v_lshlrev_b32_e32 v216, 16, v219
	v_mul_f32_e32 v207, 0xbfb8aa3b, v210
	v_min_f32_e32 v212, 0x49800000, v212
	v_exp_f32_e32 v214, v214
	v_mul_f32_e32 v211, 0xbfb8aa3b, v211
	v_exp_f32_e32 v210, v207
	v_mov_b32_e32 v207, v208
	v_add_f32_e32 v208, 1.0, v218
	v_exp_f32_e32 v218, v211
	v_mul_f32_e32 v216, 0xbfb8aa3b, v216
	v_exp_f32_e32 v216, v216
	v_add_f32_e32 v211, 1.0, v214
	v_mul_f32_e32 v206, 0xbfb8aa3b, v206
	v_and_b32_e32 v217, 0xffff0000, v219
	v_min_f32_e32 v214, 0x49800000, v211
	v_mov_b32_e32 v211, v212
	v_add_f32_e32 v212, 1.0, v218
	v_mul_f32_e32 v218, 0xbfb8aa3b, v220
	v_exp_f32_e32 v206, v206
	v_mul_f32_e32 v215, 0xbfb8aa3b, v215
	v_exp_f32_e32 v218, v218
	v_add_f32_e32 v216, 1.0, v216
	v_mul_f32_e32 v217, 0xbfb8aa3b, v217
	v_exp_f32_e32 v215, v215
	v_min_f32_e32 v219, 0x49800000, v216
	v_exp_f32_e32 v217, v217
	v_mul_f32_e32 v204, 0xbfb8aa3b, v204
	v_add_f32_e32 v206, 1.0, v206
	v_mul_f32_e32 v205, 0xbfb8aa3b, v205
	v_add_f32_e32 v210, 1.0, v210
	v_mul_f32_e32 v209, 0xbfb8aa3b, v209
	v_add_f32_e32 v218, 1.0, v218
	v_exp_f32_e32 v204, v204
	v_min_f32_e32 v206, 0x49800000, v206
	v_exp_f32_e32 v205, v205
	v_min_f32_e32 v210, 0x49800000, v210
	v_exp_f32_e32 v209, v209
	v_mul_f32_e32 v213, 0xbfb8aa3b, v213
	v_add_f32_e32 v215, 1.0, v215
	v_rcp_f32_e32 v216, v218
	v_mov_b32_e32 v218, v219
	v_mul_f32_e32 v219, 0xbfb8aa3b, v221
	v_add_f32_e32 v217, 1.0, v217
	v_exp_f32_e32 v213, v213
	v_min_f32_e32 v215, 0x49800000, v215
	v_exp_f32_e32 v219, v219
	v_min_f32_e32 v220, 0x49800000, v217
	v_add_f32_e32 v204, 1.0, v204
	v_add_f32_e32 v205, 1.0, v205
	v_add_f32_e32 v209, 1.0, v209
	v_rcp_f32_e32 v204, v204
	v_rcp_f32_e32 v205, v205
	v_rcp_f32_e32 v208, v208
	v_rcp_f32_e32 v209, v209
	v_add_f32_e32 v213, 1.0, v213
	v_add_f32_e32 v217, 1.0, v219
	v_mov_b32_e32 v219, v220
	v_rcp_f32_e32 v212, v212
	v_rcp_f32_e32 v213, v213
	v_rcp_f32_e32 v217, v217
	v_pk_mul_f32 v[204:205], v[204:205], v[206:207]
	v_pk_mul_f32 v[206:207], v[208:209], v[210:211]
	v_pk_mul_f32 v[208:209], v[212:213], v[214:215]
	v_pk_mul_f32 v[210:211], v[216:217], v[218:219]
	v_pk_mul_f32 v[118:119], v[118:119], v[206:207]
	s_waitcnt vmcnt(8)
	v_lshlrev_b32_e32 v206, 16, v142
	v_and_b32_e32 v207, 0xffff0000, v142
	s_waitcnt vmcnt(6)
	v_lshlrev_b32_e32 v142, 16, v136
	v_pk_mul_f32 v[114:115], v[114:115], v[210:211]
	v_pk_mul_f32 v[112:113], v[112:113], v[208:209]
	v_lshlrev_b32_e32 v208, 16, v143
	v_and_b32_e32 v209, 0xffff0000, v143
	v_and_b32_e32 v143, 0xffff0000, v136
	v_lshlrev_b32_e32 v210, 16, v137
	v_and_b32_e32 v211, 0xffff0000, v137
	v_mul_f32_e32 v137, 0xbfb8aa3b, v142
	v_lshlrev_b32_e32 v212, 16, v138
	v_and_b32_e32 v213, 0xffff0000, v138
	v_exp_f32_e32 v137, v137
	v_mul_f32_e32 v138, 0xbfb8aa3b, v143
	v_exp_f32_e32 v138, v138
	v_pk_mul_f32 v[116:117], v[116:117], v[204:205]
	v_lshlrev_b32_e32 v204, 16, v140
	v_and_b32_e32 v140, 0xffff0000, v140
	v_add_f32_e32 v137, 1.0, v137
	v_mul_f32_e32 v136, 0xbfb8aa3b, v204
	v_lshlrev_b32_e32 v214, 16, v139
	v_and_b32_e32 v215, 0xffff0000, v139
	v_min_f32_e32 v137, 0x49800000, v137
	v_mul_f32_e32 v139, 0xbfb8aa3b, v140
	v_add_f32_e32 v138, 1.0, v138
	v_mul_f32_e32 v204, 0xbfb8aa3b, v212
	v_exp_f32_e32 v139, v139
	v_min_f32_e32 v140, 0x49800000, v138
	v_exp_f32_e32 v204, v204
	v_lshlrev_b32_e32 v205, 16, v141
	v_mov_b32_e32 v138, v137
	v_add_f32_e32 v137, 1.0, v139
	v_mov_b32_e32 v139, v140
	v_mul_f32_e32 v140, 0xbfb8aa3b, v205
	v_mul_f32_e32 v205, 0xbfb8aa3b, v206
	v_add_f32_e32 v204, 1.0, v204
	v_exp_f32_e32 v205, v205
	v_min_f32_e32 v206, 0x49800000, v204
	v_mul_f32_e32 v142, 0xbfb8aa3b, v210
	v_mul_f32_e32 v143, 0xbfb8aa3b, v211
	v_add_f32_e32 v204, 1.0, v205
	v_mov_b32_e32 v205, v206
	v_mul_f32_e32 v206, 0xbfb8aa3b, v207
	v_exp_f32_e32 v207, v206
	v_mul_f32_e32 v206, 0xbfb8aa3b, v213
	v_exp_f32_e32 v210, v206
	v_mov_b32_e32 v206, v205
	v_add_f32_e32 v205, 1.0, v207
	v_mul_f32_e32 v211, 0xbfb8aa3b, v215
	v_add_f32_e32 v207, 1.0, v210
	v_mul_f32_e32 v210, 0xbfb8aa3b, v214
	v_exp_f32_e32 v142, v142
	v_exp_f32_e32 v143, v143
	v_exp_f32_e32 v210, v210
	v_exp_f32_e32 v211, v211
	v_and_b32_e32 v141, 0xffff0000, v141
	v_add_f32_e32 v142, 1.0, v142
	v_mul_f32_e32 v141, 0xbfb8aa3b, v141
	v_add_f32_e32 v143, 1.0, v143
	v_mul_f32_e32 v208, 0xbfb8aa3b, v208
	v_add_f32_e32 v210, 1.0, v210
	v_mul_f32_e32 v209, 0xbfb8aa3b, v209
	v_add_f32_e32 v211, 1.0, v211
	v_exp_f32_e32 v136, v136
	v_exp_f32_e32 v140, v140
	v_min_f32_e32 v142, 0x49800000, v142
	v_exp_f32_e32 v141, v141
	v_min_f32_e32 v143, 0x49800000, v143
	v_min_f32_e32 v207, 0x49800000, v207
	v_exp_f32_e32 v208, v208
	v_min_f32_e32 v210, 0x49800000, v210
	v_exp_f32_e32 v209, v209
	v_min_f32_e32 v211, 0x49800000, v211
	v_add_f32_e32 v136, 1.0, v136
	v_add_f32_e32 v140, 1.0, v140
	v_add_f32_e32 v141, 1.0, v141
	v_add_f32_e32 v208, 1.0, v208
	v_add_f32_e32 v209, 1.0, v209
	v_rcp_f32_e32 v136, v136
	v_rcp_f32_e32 v137, v137
	v_rcp_f32_e32 v140, v140
	v_rcp_f32_e32 v141, v141
	v_rcp_f32_e32 v204, v204
	v_rcp_f32_e32 v205, v205
	v_rcp_f32_e32 v208, v208
	v_rcp_f32_e32 v209, v209
	v_pk_mul_f32 v[136:137], v[136:137], v[138:139]
	v_pk_mul_f32 v[138:139], v[140:141], v[142:143]
	v_pk_mul_f32 v[140:141], v[204:205], v[206:207]
	v_pk_mul_f32 v[142:143], v[208:209], v[210:211]
	global_load_dwordx4 v[204:207], v[182:183], off
	global_load_dwordx4 v[208:211], v[174:175], off
	v_pk_mul_f32 v[110:111], v[110:111], v[138:139]
	v_lshlrev_b32_e32 v138, 16, v134
	v_and_b32_e32 v139, 0xffff0000, v134
	s_waitcnt vmcnt(7)
	v_lshlrev_b32_e32 v134, 16, v128
	v_pk_mul_f32 v[104:105], v[104:105], v[140:141]
	v_lshlrev_b32_e32 v140, 16, v135
	v_and_b32_e32 v141, 0xffff0000, v135
	v_and_b32_e32 v135, 0xffff0000, v128
	v_mul_f32_e32 v128, 0xbfb8aa3b, v134
	v_exp_f32_e32 v128, v128
	v_pk_mul_f32 v[108:109], v[108:109], v[136:137]
	v_lshlrev_b32_e32 v136, 16, v132
	v_pk_mul_f32 v[106:107], v[106:107], v[142:143]
	v_lshlrev_b32_e32 v142, 16, v129
	v_and_b32_e32 v143, 0xffff0000, v129
	v_lshlrev_b32_e32 v212, 16, v130
	v_mul_f32_e32 v129, 0xbfb8aa3b, v136
	v_add_f32_e32 v128, 1.0, v128
	v_and_b32_e32 v213, 0xffff0000, v130
	v_exp_f32_e32 v129, v129
	v_min_f32_e32 v130, 0x49800000, v128
	v_mul_f32_e32 v136, 0xbfb8aa3b, v212
	v_exp_f32_e32 v136, v136
	v_and_b32_e32 v132, 0xffff0000, v132
	v_lshlrev_b32_e32 v137, 16, v133
	v_add_f32_e32 v128, 1.0, v129
	v_mov_b32_e32 v129, v130
	v_mul_f32_e32 v130, 0xbfb8aa3b, v135
	v_lshlrev_b32_e32 v214, 16, v131
	v_and_b32_e32 v215, 0xffff0000, v131
	v_exp_f32_e32 v131, v130
	v_mov_b32_e32 v130, v129
	v_mul_f32_e32 v129, 0xbfb8aa3b, v132
	v_mul_f32_e32 v132, 0xbfb8aa3b, v137
	v_mul_f32_e32 v137, 0xbfb8aa3b, v138
	v_add_f32_e32 v136, 1.0, v136
	v_exp_f32_e32 v137, v137
	v_min_f32_e32 v138, 0x49800000, v136
	v_mul_f32_e32 v134, 0xbfb8aa3b, v142
	v_mul_f32_e32 v135, 0xbfb8aa3b, v143
	v_add_f32_e32 v136, 1.0, v137
	v_mov_b32_e32 v137, v138
	v_mul_f32_e32 v138, 0xbfb8aa3b, v139
	v_exp_f32_e32 v139, v138
	v_mul_f32_e32 v138, 0xbfb8aa3b, v213
	v_exp_f32_e32 v142, v138
	v_mov_b32_e32 v138, v137
	v_add_f32_e32 v137, 1.0, v139
	v_mul_f32_e32 v143, 0xbfb8aa3b, v215
	v_add_f32_e32 v139, 1.0, v142
	v_mul_f32_e32 v142, 0xbfb8aa3b, v214
	v_exp_f32_e32 v134, v134
	v_exp_f32_e32 v135, v135
	v_exp_f32_e32 v142, v142
	v_exp_f32_e32 v143, v143
	v_and_b32_e32 v133, 0xffff0000, v133
	v_add_f32_e32 v131, 1.0, v131
	v_add_f32_e32 v134, 1.0, v134
	v_mul_f32_e32 v133, 0xbfb8aa3b, v133
	v_add_f32_e32 v135, 1.0, v135
	v_mul_f32_e32 v140, 0xbfb8aa3b, v140
	v_add_f32_e32 v142, 1.0, v142
	v_mul_f32_e32 v141, 0xbfb8aa3b, v141
	v_add_f32_e32 v143, 1.0, v143
	v_exp_f32_e32 v129, v129
	v_min_f32_e32 v131, 0x49800000, v131
	v_exp_f32_e32 v132, v132
	v_min_f32_e32 v134, 0x49800000, v134
	v_exp_f32_e32 v133, v133
	v_min_f32_e32 v135, 0x49800000, v135
	v_min_f32_e32 v139, 0x49800000, v139
	v_exp_f32_e32 v140, v140
	v_min_f32_e32 v142, 0x49800000, v142
	v_exp_f32_e32 v141, v141
	v_min_f32_e32 v143, 0x49800000, v143
	v_add_f32_e32 v129, 1.0, v129
	v_add_f32_e32 v132, 1.0, v132
	v_add_f32_e32 v133, 1.0, v133
	v_add_f32_e32 v140, 1.0, v140
	v_add_f32_e32 v141, 1.0, v141
	v_rcp_f32_e32 v128, v128
	v_rcp_f32_e32 v129, v129
	v_rcp_f32_e32 v132, v132
	v_rcp_f32_e32 v133, v133
	v_rcp_f32_e32 v136, v136
	v_rcp_f32_e32 v137, v137
	v_rcp_f32_e32 v140, v140
	v_rcp_f32_e32 v141, v141
	v_pk_mul_f32 v[128:129], v[128:129], v[130:131]
	v_pk_mul_f32 v[130:131], v[132:133], v[134:135]
	v_pk_mul_f32 v[132:133], v[136:137], v[138:139]
	v_pk_mul_f32 v[134:135], v[140:141], v[142:143]
	v_pk_mul_f32 v[102:103], v[102:103], v[130:131]
	v_pk_mul_f32 v[100:101], v[100:101], v[128:129]
	v_pk_mul_f32 v[98:99], v[98:99], v[134:135]
	v_pk_mul_f32 v[96:97], v[96:97], v[132:133]
	global_load_dwordx4 v[212:215], v[186:187], off offset:256
	global_load_dwordx4 v[216:219], v[158:159], off offset:256
	global_load_dwordx4 v[140:143], v[188:189], off
	global_load_dwordx4 v[132:135], v[188:189], off offset:256
	global_load_dwordx4 v[136:139], v[160:161], off
	global_load_dwordx4 v[128:131], v[176:177], off offset:256
	s_waitcnt vmcnt(7)
	v_lshlrev_b32_e32 v220, 16, v204
	v_and_b32_e32 v221, 0xffff0000, v204
	s_waitcnt vmcnt(6)
	v_lshlrev_b32_e32 v204, 16, v208
	v_mul_f32_e32 v204, 0xbfb8aa3b, v204
	v_exp_f32_e32 v204, v204
	v_lshlrev_b32_e32 v222, 16, v205
	v_and_b32_e32 v223, 0xffff0000, v205
	v_lshlrev_b32_e32 v224, 16, v206
	v_and_b32_e32 v225, 0xffff0000, v206
	v_and_b32_e32 v205, 0xffff0000, v208
	v_mul_f32_e32 v206, 0xbfb8aa3b, v220
	v_exp_f32_e32 v206, v206
	v_add_f32_e32 v204, 1.0, v204
	v_mul_f32_e32 v205, 0xbfb8aa3b, v205
	v_min_f32_e32 v208, 0x49800000, v204
	v_exp_f32_e32 v205, v205
	v_add_f32_e32 v206, 1.0, v206
	v_rcp_f32_e32 v204, v206
	v_mov_b32_e32 v206, v208
	v_mul_f32_e32 v208, 0xbfb8aa3b, v221
	v_add_f32_e32 v205, 1.0, v205
	v_lshlrev_b32_e32 v228, 16, v210
	v_and_b32_e32 v229, 0xffff0000, v210
	v_exp_f32_e32 v208, v208
	v_min_f32_e32 v210, 0x49800000, v205
	v_lshlrev_b32_e32 v226, 16, v207
	v_and_b32_e32 v227, 0xffff0000, v207
	v_lshlrev_b32_e32 v207, 16, v209
	v_add_f32_e32 v205, 1.0, v208
	v_mov_b32_e32 v208, v210
	v_mul_f32_e32 v210, 0xbfb8aa3b, v222
	v_mul_f32_e32 v207, 0xbfb8aa3b, v207
	v_lshlrev_b32_e32 v230, 16, v211
	v_and_b32_e32 v231, 0xffff0000, v211
	v_exp_f32_e32 v210, v210
	v_exp_f32_e32 v211, v207
	v_and_b32_e32 v209, 0xffff0000, v209
	v_mov_b32_e32 v207, v208
	v_add_f32_e32 v208, 1.0, v210
	v_add_f32_e32 v210, 1.0, v211
	v_mul_f32_e32 v211, 0xbfb8aa3b, v223
	v_mul_f32_e32 v209, 0xbfb8aa3b, v209
	v_exp_f32_e32 v211, v211
	v_exp_f32_e32 v209, v209
	v_mul_f32_e32 v221, 0xbfb8aa3b, v224
	v_exp_f32_e32 v221, v221
	v_add_f32_e32 v211, 1.0, v211
	v_add_f32_e32 v209, 1.0, v209
	v_min_f32_e32 v220, 0x49800000, v209
	v_rcp_f32_e32 v209, v211
	v_mul_f32_e32 v211, 0xbfb8aa3b, v228
	v_exp_f32_e32 v211, v211
	v_min_f32_e32 v210, 0x49800000, v210
	v_add_f32_e32 v211, 1.0, v211
	v_min_f32_e32 v222, 0x49800000, v211
	v_mov_b32_e32 v211, v220
	v_add_f32_e32 v220, 1.0, v221
	v_mov_b32_e32 v221, v222
	v_mul_f32_e32 v222, 0xbfb8aa3b, v225
	v_exp_f32_e32 v223, v222
	v_mul_f32_e32 v222, 0xbfb8aa3b, v229
	v_exp_f32_e32 v224, v222
	v_mov_b32_e32 v222, v221
	v_add_f32_e32 v221, 1.0, v223
	v_mul_f32_e32 v225, 0xbfb8aa3b, v230
	v_add_f32_e32 v223, 1.0, v224
	v_min_f32_e32 v223, 0x49800000, v223
	v_mul_f32_e32 v224, 0xbfb8aa3b, v226
	v_exp_f32_e32 v225, v225
	v_mul_f32_e32 v226, 0xbfb8aa3b, v231
	v_exp_f32_e32 v226, v226
	v_rcp_f32_e32 v205, v205
	v_rcp_f32_e32 v208, v208
	v_rcp_f32_e32 v220, v220
	v_rcp_f32_e32 v221, v221
	v_add_f32_e32 v225, 1.0, v225
	v_min_f32_e32 v225, 0x49800000, v225
	v_mul_f32_e32 v227, 0xbfb8aa3b, v227
	v_add_f32_e32 v226, 1.0, v226
	v_exp_f32_e32 v224, v224
	v_exp_f32_e32 v227, v227
	v_min_f32_e32 v228, 0x49800000, v226
	v_pk_mul_f32 v[204:205], v[204:205], v[206:207]
	v_pk_mul_f32 v[206:207], v[208:209], v[210:211]
	v_pk_mul_f32 v[208:209], v[220:221], v[222:223]
	v_pk_mul_f32 v[88:89], v[88:89], v[208:209]
	s_waitcnt vmcnt(11)
	v_and_b32_e32 v208, 0xffff0000, v236
	v_mul_f32_e32 v208, 0xbfb8aa3b, v208
	v_add_f32_e32 v224, 1.0, v224
	v_mov_b32_e32 v226, v225
	v_add_f32_e32 v225, 1.0, v227
	v_mov_b32_e32 v227, v228
	v_exp_f32_e32 v208, v208
	v_rcp_f32_e32 v224, v224
	v_rcp_f32_e32 v225, v225
	v_pk_mul_f32 v[92:93], v[92:93], v[204:205]
	v_lshlrev_b32_e32 v204, 16, v232
	v_and_b32_e32 v205, 0xffff0000, v232
	v_and_b32_e32 v232, 0xffff0000, v237
	v_mul_f32_e32 v232, 0xbfb8aa3b, v232
	v_pk_mul_f32 v[94:95], v[94:95], v[206:207]
	v_lshlrev_b32_e32 v207, 16, v233
	v_add_f32_e32 v208, 1.0, v208
	v_exp_f32_e32 v232, v232
	v_pk_mul_f32 v[210:211], v[224:225], v[226:227]
	v_min_f32_e32 v208, 0x49800000, v208
	v_mul_f32_e32 v207, 0xbfb8aa3b, v207
	v_pk_mul_f32 v[90:91], v[90:91], v[210:211]
	v_and_b32_e32 v209, 0xffff0000, v233
	v_lshlrev_b32_e32 v211, 16, v234
	v_and_b32_e32 v233, 0xffff0000, v234
	v_lshlrev_b32_e32 v220, 16, v235
	v_and_b32_e32 v221, 0xffff0000, v235
	v_lshlrev_b32_e32 v234, 16, v238
	v_and_b32_e32 v235, 0xffff0000, v238
	v_exp_f32_e32 v238, v207
	v_lshlrev_b32_e32 v210, 16, v237
	v_add_f32_e32 v232, 1.0, v232
	v_mul_f32_e32 v234, 0xbfb8aa3b, v234
	v_lshlrev_b32_e32 v206, 16, v236
	v_lshlrev_b32_e32 v236, 16, v239
	v_mul_f32_e32 v207, 0xbfb8aa3b, v210
	v_min_f32_e32 v232, 0x49800000, v232
	v_exp_f32_e32 v234, v234
	v_mul_f32_e32 v211, 0xbfb8aa3b, v211
	v_exp_f32_e32 v210, v207
	v_mov_b32_e32 v207, v208
	v_add_f32_e32 v208, 1.0, v238
	v_exp_f32_e32 v238, v211
	v_mul_f32_e32 v236, 0xbfb8aa3b, v236
	v_exp_f32_e32 v236, v236
	v_add_f32_e32 v211, 1.0, v234
	v_mul_f32_e32 v206, 0xbfb8aa3b, v206
	v_and_b32_e32 v237, 0xffff0000, v239
	v_min_f32_e32 v234, 0x49800000, v211
	v_mov_b32_e32 v211, v232
	v_add_f32_e32 v232, 1.0, v238
	v_mul_f32_e32 v238, 0xbfb8aa3b, v220
	v_exp_f32_e32 v206, v206
	v_mul_f32_e32 v235, 0xbfb8aa3b, v235
	v_exp_f32_e32 v238, v238
	v_add_f32_e32 v236, 1.0, v236
	v_mul_f32_e32 v237, 0xbfb8aa3b, v237
	v_exp_f32_e32 v235, v235
	v_min_f32_e32 v239, 0x49800000, v236
	v_exp_f32_e32 v237, v237
	v_mul_f32_e32 v204, 0xbfb8aa3b, v204
	v_add_f32_e32 v206, 1.0, v206
	v_mul_f32_e32 v205, 0xbfb8aa3b, v205
	v_add_f32_e32 v210, 1.0, v210
	v_mul_f32_e32 v209, 0xbfb8aa3b, v209
	v_add_f32_e32 v238, 1.0, v238
	v_exp_f32_e32 v204, v204
	v_min_f32_e32 v206, 0x49800000, v206
	v_exp_f32_e32 v205, v205
	v_min_f32_e32 v210, 0x49800000, v210
	v_exp_f32_e32 v209, v209
	v_mul_f32_e32 v233, 0xbfb8aa3b, v233
	v_add_f32_e32 v235, 1.0, v235
	v_rcp_f32_e32 v236, v238
	v_mov_b32_e32 v238, v239
	v_mul_f32_e32 v239, 0xbfb8aa3b, v221
	v_add_f32_e32 v237, 1.0, v237
	v_exp_f32_e32 v233, v233
	v_min_f32_e32 v235, 0x49800000, v235
	v_exp_f32_e32 v239, v239
	v_min_f32_e32 v220, 0x49800000, v237
	v_add_f32_e32 v204, 1.0, v204
	v_add_f32_e32 v205, 1.0, v205
	v_add_f32_e32 v209, 1.0, v209
	v_rcp_f32_e32 v204, v204
	v_rcp_f32_e32 v205, v205
	v_rcp_f32_e32 v208, v208
	v_rcp_f32_e32 v209, v209
	v_add_f32_e32 v233, 1.0, v233
	v_add_f32_e32 v237, 1.0, v239
	v_mov_b32_e32 v239, v220
	v_rcp_f32_e32 v232, v232
	v_rcp_f32_e32 v233, v233
	v_rcp_f32_e32 v237, v237
	v_pk_mul_f32 v[204:205], v[204:205], v[206:207]
	v_pk_mul_f32 v[206:207], v[208:209], v[210:211]
	v_pk_mul_f32 v[208:209], v[232:233], v[234:235]
	v_pk_mul_f32 v[210:211], v[236:237], v[238:239]
	v_pk_mul_f32 v[86:87], v[86:87], v[206:207]
	s_waitcnt vmcnt(10)
	v_lshlrev_b32_e32 v206, 16, v242
	v_and_b32_e32 v207, 0xffff0000, v242
	s_waitcnt vmcnt(8)
	v_lshlrev_b32_e32 v242, 16, v248
	v_pk_mul_f32 v[82:83], v[82:83], v[210:211]
	v_pk_mul_f32 v[80:81], v[80:81], v[208:209]
	v_lshlrev_b32_e32 v208, 16, v243
	v_and_b32_e32 v209, 0xffff0000, v243
	v_and_b32_e32 v243, 0xffff0000, v248
	v_lshlrev_b32_e32 v210, 16, v249
	v_and_b32_e32 v211, 0xffff0000, v249
	v_mul_f32_e32 v249, 0xbfb8aa3b, v242
	v_lshlrev_b32_e32 v232, 16, v250
	v_and_b32_e32 v233, 0xffff0000, v250
	v_exp_f32_e32 v249, v249
	v_mul_f32_e32 v250, 0xbfb8aa3b, v243
	v_exp_f32_e32 v250, v250
	v_pk_mul_f32 v[84:85], v[84:85], v[204:205]
	v_lshlrev_b32_e32 v204, 16, v240
	v_and_b32_e32 v240, 0xffff0000, v240
	v_add_f32_e32 v249, 1.0, v249
	v_mul_f32_e32 v248, 0xbfb8aa3b, v204
	v_lshlrev_b32_e32 v234, 16, v251
	v_and_b32_e32 v235, 0xffff0000, v251
	v_min_f32_e32 v249, 0x49800000, v249
	v_mul_f32_e32 v251, 0xbfb8aa3b, v240
	v_add_f32_e32 v250, 1.0, v250
	v_mul_f32_e32 v204, 0xbfb8aa3b, v232
	v_exp_f32_e32 v251, v251
	v_min_f32_e32 v240, 0x49800000, v250
	v_exp_f32_e32 v204, v204
	v_lshlrev_b32_e32 v205, 16, v241
	v_mov_b32_e32 v250, v249
	v_add_f32_e32 v249, 1.0, v251
	v_mov_b32_e32 v251, v240
	v_mul_f32_e32 v240, 0xbfb8aa3b, v205
	v_mul_f32_e32 v205, 0xbfb8aa3b, v206
	v_add_f32_e32 v204, 1.0, v204
	v_exp_f32_e32 v205, v205
	v_min_f32_e32 v206, 0x49800000, v204
	v_mul_f32_e32 v242, 0xbfb8aa3b, v210
	v_mul_f32_e32 v243, 0xbfb8aa3b, v211
	v_add_f32_e32 v204, 1.0, v205
	v_mov_b32_e32 v205, v206
	v_mul_f32_e32 v206, 0xbfb8aa3b, v207
	v_exp_f32_e32 v207, v206
	v_mul_f32_e32 v206, 0xbfb8aa3b, v233
	v_exp_f32_e32 v210, v206
	v_mov_b32_e32 v206, v205
	v_add_f32_e32 v205, 1.0, v207
	v_mul_f32_e32 v211, 0xbfb8aa3b, v235
	v_add_f32_e32 v207, 1.0, v210
	v_mul_f32_e32 v210, 0xbfb8aa3b, v234
	v_exp_f32_e32 v242, v242
	v_exp_f32_e32 v243, v243
	v_exp_f32_e32 v210, v210
	v_exp_f32_e32 v211, v211
	v_and_b32_e32 v241, 0xffff0000, v241
	v_add_f32_e32 v242, 1.0, v242
	v_mul_f32_e32 v241, 0xbfb8aa3b, v241
	v_add_f32_e32 v243, 1.0, v243
	v_mul_f32_e32 v208, 0xbfb8aa3b, v208
	v_add_f32_e32 v210, 1.0, v210
	v_mul_f32_e32 v209, 0xbfb8aa3b, v209
	v_add_f32_e32 v211, 1.0, v211
	v_exp_f32_e32 v248, v248
	v_exp_f32_e32 v240, v240
	v_min_f32_e32 v242, 0x49800000, v242
	v_exp_f32_e32 v241, v241
	v_min_f32_e32 v243, 0x49800000, v243
	v_min_f32_e32 v207, 0x49800000, v207
	v_exp_f32_e32 v208, v208
	v_min_f32_e32 v210, 0x49800000, v210
	v_exp_f32_e32 v209, v209
	v_min_f32_e32 v211, 0x49800000, v211
	v_add_f32_e32 v248, 1.0, v248
	v_add_f32_e32 v240, 1.0, v240
	v_add_f32_e32 v241, 1.0, v241
	v_add_f32_e32 v208, 1.0, v208
	v_add_f32_e32 v209, 1.0, v209
	v_rcp_f32_e32 v248, v248
	v_rcp_f32_e32 v249, v249
	v_rcp_f32_e32 v240, v240
	v_rcp_f32_e32 v241, v241
	v_rcp_f32_e32 v204, v204
	v_rcp_f32_e32 v205, v205
	v_rcp_f32_e32 v208, v208
	v_rcp_f32_e32 v209, v209
	v_pk_mul_f32 v[248:249], v[248:249], v[250:251]
	v_pk_mul_f32 v[250:251], v[240:241], v[242:243]
	v_pk_mul_f32 v[240:241], v[204:205], v[206:207]
	v_pk_mul_f32 v[242:243], v[208:209], v[210:211]
	global_load_dwordx4 v[204:207], v[186:187], off
	global_load_dwordx4 v[208:211], v[158:159], off
	v_pk_mul_f32 v[78:79], v[78:79], v[250:251]
	v_lshlrev_b32_e32 v250, 16, v246
	v_and_b32_e32 v251, 0xffff0000, v246
	s_waitcnt vmcnt(2)
	v_lshlrev_b32_e32 v246, 16, v128
	v_pk_mul_f32 v[72:73], v[72:73], v[240:241]
	v_lshlrev_b32_e32 v240, 16, v247
	v_and_b32_e32 v241, 0xffff0000, v247
	v_and_b32_e32 v247, 0xffff0000, v128
	v_mul_f32_e32 v128, 0xbfb8aa3b, v246
	v_exp_f32_e32 v128, v128
	v_pk_mul_f32 v[76:77], v[76:77], v[248:249]
	v_lshlrev_b32_e32 v248, 16, v244
	v_pk_mul_f32 v[74:75], v[74:75], v[242:243]
	v_lshlrev_b32_e32 v242, 16, v129
	v_and_b32_e32 v243, 0xffff0000, v129
	v_lshlrev_b32_e32 v232, 16, v130
	v_mul_f32_e32 v129, 0xbfb8aa3b, v248
	v_add_f32_e32 v128, 1.0, v128
	v_and_b32_e32 v233, 0xffff0000, v130
	v_exp_f32_e32 v129, v129
	v_min_f32_e32 v130, 0x49800000, v128
	v_mul_f32_e32 v248, 0xbfb8aa3b, v232
	v_exp_f32_e32 v248, v248
	v_and_b32_e32 v244, 0xffff0000, v244
	v_lshlrev_b32_e32 v249, 16, v245
	v_add_f32_e32 v128, 1.0, v129
	v_mov_b32_e32 v129, v130
	v_mul_f32_e32 v130, 0xbfb8aa3b, v247
	v_lshlrev_b32_e32 v234, 16, v131
	v_and_b32_e32 v235, 0xffff0000, v131
	v_exp_f32_e32 v131, v130
	v_mov_b32_e32 v130, v129
	v_mul_f32_e32 v129, 0xbfb8aa3b, v244
	v_mul_f32_e32 v244, 0xbfb8aa3b, v249
	v_mul_f32_e32 v249, 0xbfb8aa3b, v250
	v_add_f32_e32 v248, 1.0, v248
	v_exp_f32_e32 v249, v249
	v_min_f32_e32 v250, 0x49800000, v248
	v_mul_f32_e32 v246, 0xbfb8aa3b, v242
	v_mul_f32_e32 v247, 0xbfb8aa3b, v243
	v_add_f32_e32 v248, 1.0, v249
	v_mov_b32_e32 v249, v250
	v_mul_f32_e32 v250, 0xbfb8aa3b, v251
	v_exp_f32_e32 v251, v250
	v_mul_f32_e32 v250, 0xbfb8aa3b, v233
	v_exp_f32_e32 v242, v250
	v_mov_b32_e32 v250, v249
	v_add_f32_e32 v249, 1.0, v251
	v_mul_f32_e32 v243, 0xbfb8aa3b, v235
	v_add_f32_e32 v251, 1.0, v242
	v_mul_f32_e32 v242, 0xbfb8aa3b, v234
	v_exp_f32_e32 v246, v246
	v_exp_f32_e32 v247, v247
	v_exp_f32_e32 v242, v242
	v_exp_f32_e32 v243, v243
	v_and_b32_e32 v245, 0xffff0000, v245
	v_add_f32_e32 v131, 1.0, v131
	v_add_f32_e32 v246, 1.0, v246
	v_mul_f32_e32 v245, 0xbfb8aa3b, v245
	v_add_f32_e32 v247, 1.0, v247
	v_mul_f32_e32 v240, 0xbfb8aa3b, v240
	v_add_f32_e32 v242, 1.0, v242
	v_mul_f32_e32 v241, 0xbfb8aa3b, v241
	v_add_f32_e32 v243, 1.0, v243
	v_exp_f32_e32 v129, v129
	v_min_f32_e32 v131, 0x49800000, v131
	v_exp_f32_e32 v244, v244
	v_min_f32_e32 v246, 0x49800000, v246
	v_exp_f32_e32 v245, v245
	v_min_f32_e32 v247, 0x49800000, v247
	v_min_f32_e32 v251, 0x49800000, v251
	v_exp_f32_e32 v240, v240
	v_min_f32_e32 v242, 0x49800000, v242
	v_exp_f32_e32 v241, v241
	v_min_f32_e32 v243, 0x49800000, v243
	v_add_f32_e32 v129, 1.0, v129
	v_add_f32_e32 v244, 1.0, v244
	v_add_f32_e32 v245, 1.0, v245
	v_add_f32_e32 v240, 1.0, v240
	v_add_f32_e32 v241, 1.0, v241
	v_rcp_f32_e32 v128, v128
	v_rcp_f32_e32 v129, v129
	v_rcp_f32_e32 v244, v244
	v_rcp_f32_e32 v245, v245
	v_rcp_f32_e32 v248, v248
	v_rcp_f32_e32 v249, v249
	v_rcp_f32_e32 v240, v240
	v_rcp_f32_e32 v241, v241
	v_pk_mul_f32 v[128:129], v[128:129], v[130:131]
	v_pk_mul_f32 v[130:131], v[244:245], v[246:247]
	v_pk_mul_f32 v[244:245], v[248:249], v[250:251]
	v_pk_mul_f32 v[246:247], v[240:241], v[242:243]
	v_pk_mul_f32 v[70:71], v[70:71], v[130:131]
	v_pk_mul_f32 v[68:69], v[68:69], v[128:129]
	v_pk_mul_f32 v[66:67], v[66:67], v[246:247]
	v_pk_mul_f32 v[64:65], v[64:65], v[244:245]
	global_load_dwordx4 v[232:235], v[190:191], off offset:256
	global_load_dwordx4 v[236:239], v[162:163], off offset:256
	global_load_dwordx4 v[240:243], v[192:193], off
	global_load_dwordx4 v[244:247], v[192:193], off offset:256
	global_load_dwordx4 v[248:251], v[164:165], off
	global_load_dwordx4 v[128:131], v[160:161], off offset:256
	s_waitcnt vmcnt(7)
	v_lshlrev_b32_e32 v220, 16, v204
	v_and_b32_e32 v221, 0xffff0000, v204
	s_waitcnt vmcnt(6)
	v_lshlrev_b32_e32 v204, 16, v208
	v_mul_f32_e32 v204, 0xbfb8aa3b, v204
	v_exp_f32_e32 v204, v204
	v_lshlrev_b32_e32 v222, 16, v205
	v_and_b32_e32 v223, 0xffff0000, v205
	v_lshlrev_b32_e32 v224, 16, v206
	v_and_b32_e32 v225, 0xffff0000, v206
	v_and_b32_e32 v205, 0xffff0000, v208
	v_mul_f32_e32 v206, 0xbfb8aa3b, v220
	v_exp_f32_e32 v206, v206
	v_add_f32_e32 v204, 1.0, v204
	v_mul_f32_e32 v205, 0xbfb8aa3b, v205
	v_min_f32_e32 v208, 0x49800000, v204
	v_exp_f32_e32 v205, v205
	v_add_f32_e32 v206, 1.0, v206
	v_rcp_f32_e32 v204, v206
	v_mov_b32_e32 v206, v208
	v_mul_f32_e32 v208, 0xbfb8aa3b, v221
	v_add_f32_e32 v205, 1.0, v205
	v_lshlrev_b32_e32 v228, 16, v210
	v_and_b32_e32 v229, 0xffff0000, v210
	v_exp_f32_e32 v208, v208
	v_min_f32_e32 v210, 0x49800000, v205
	v_lshlrev_b32_e32 v226, 16, v207
	v_and_b32_e32 v227, 0xffff0000, v207
	v_lshlrev_b32_e32 v207, 16, v209
	v_add_f32_e32 v205, 1.0, v208
	v_mov_b32_e32 v208, v210
	v_mul_f32_e32 v210, 0xbfb8aa3b, v222
	v_mul_f32_e32 v207, 0xbfb8aa3b, v207
	v_lshlrev_b32_e32 v230, 16, v211
	v_and_b32_e32 v231, 0xffff0000, v211
	v_exp_f32_e32 v210, v210
	v_exp_f32_e32 v211, v207
	v_and_b32_e32 v209, 0xffff0000, v209
	v_mov_b32_e32 v207, v208
	v_add_f32_e32 v208, 1.0, v210
	v_add_f32_e32 v210, 1.0, v211
	v_mul_f32_e32 v211, 0xbfb8aa3b, v223
	v_mul_f32_e32 v209, 0xbfb8aa3b, v209
	v_exp_f32_e32 v211, v211
	v_exp_f32_e32 v209, v209
	v_mul_f32_e32 v221, 0xbfb8aa3b, v224
	v_exp_f32_e32 v221, v221
	v_add_f32_e32 v211, 1.0, v211
	v_add_f32_e32 v209, 1.0, v209
	v_min_f32_e32 v220, 0x49800000, v209
	v_rcp_f32_e32 v209, v211
	v_mul_f32_e32 v211, 0xbfb8aa3b, v228
	v_exp_f32_e32 v211, v211
	v_min_f32_e32 v210, 0x49800000, v210
	v_add_f32_e32 v211, 1.0, v211
	v_min_f32_e32 v222, 0x49800000, v211
	v_mov_b32_e32 v211, v220
	v_add_f32_e32 v220, 1.0, v221
	v_mov_b32_e32 v221, v222
	v_mul_f32_e32 v222, 0xbfb8aa3b, v225
	v_exp_f32_e32 v223, v222
	v_mul_f32_e32 v222, 0xbfb8aa3b, v229
	v_exp_f32_e32 v224, v222
	v_mov_b32_e32 v222, v221
	v_add_f32_e32 v221, 1.0, v223
	v_mul_f32_e32 v225, 0xbfb8aa3b, v230
	v_add_f32_e32 v223, 1.0, v224
	v_min_f32_e32 v223, 0x49800000, v223
	v_mul_f32_e32 v224, 0xbfb8aa3b, v226
	v_exp_f32_e32 v225, v225
	v_mul_f32_e32 v226, 0xbfb8aa3b, v231
	v_exp_f32_e32 v226, v226
	v_rcp_f32_e32 v205, v205
	v_rcp_f32_e32 v208, v208
	v_rcp_f32_e32 v220, v220
	v_rcp_f32_e32 v221, v221
	v_add_f32_e32 v225, 1.0, v225
	v_min_f32_e32 v225, 0x49800000, v225
	v_mul_f32_e32 v227, 0xbfb8aa3b, v227
	v_add_f32_e32 v226, 1.0, v226
	v_exp_f32_e32 v224, v224
	v_exp_f32_e32 v227, v227
	v_min_f32_e32 v228, 0x49800000, v226
	v_pk_mul_f32 v[204:205], v[204:205], v[206:207]
	v_pk_mul_f32 v[206:207], v[208:209], v[210:211]
	v_pk_mul_f32 v[208:209], v[220:221], v[222:223]
	v_pk_mul_f32 v[56:57], v[56:57], v[208:209]
	s_waitcnt vmcnt(12)
	v_and_b32_e32 v208, 0xffff0000, v216
	v_mul_f32_e32 v208, 0xbfb8aa3b, v208
	v_add_f32_e32 v224, 1.0, v224
	v_mov_b32_e32 v226, v225
	v_add_f32_e32 v225, 1.0, v227
	v_mov_b32_e32 v227, v228
	v_exp_f32_e32 v208, v208
	v_rcp_f32_e32 v224, v224
	v_rcp_f32_e32 v225, v225
	v_pk_mul_f32 v[60:61], v[60:61], v[204:205]
	v_lshlrev_b32_e32 v204, 16, v212
	v_and_b32_e32 v205, 0xffff0000, v212
	v_and_b32_e32 v212, 0xffff0000, v217
	v_mul_f32_e32 v212, 0xbfb8aa3b, v212
	v_pk_mul_f32 v[62:63], v[62:63], v[206:207]
	v_lshlrev_b32_e32 v207, 16, v213
	v_add_f32_e32 v208, 1.0, v208
	v_exp_f32_e32 v212, v212
	v_pk_mul_f32 v[210:211], v[224:225], v[226:227]
	v_min_f32_e32 v208, 0x49800000, v208
	v_mul_f32_e32 v207, 0xbfb8aa3b, v207
	v_pk_mul_f32 v[58:59], v[58:59], v[210:211]
	v_and_b32_e32 v209, 0xffff0000, v213
	v_lshlrev_b32_e32 v211, 16, v214
	v_and_b32_e32 v213, 0xffff0000, v214
	v_lshlrev_b32_e32 v220, 16, v215
	v_and_b32_e32 v221, 0xffff0000, v215
	v_lshlrev_b32_e32 v214, 16, v218
	v_and_b32_e32 v215, 0xffff0000, v218
	v_exp_f32_e32 v218, v207
	v_lshlrev_b32_e32 v210, 16, v217
	v_add_f32_e32 v212, 1.0, v212
	v_mul_f32_e32 v214, 0xbfb8aa3b, v214
	v_lshlrev_b32_e32 v206, 16, v216
	v_lshlrev_b32_e32 v216, 16, v219
	v_mul_f32_e32 v207, 0xbfb8aa3b, v210
	v_min_f32_e32 v212, 0x49800000, v212
	v_exp_f32_e32 v214, v214
	v_mul_f32_e32 v211, 0xbfb8aa3b, v211
	v_exp_f32_e32 v210, v207
	v_mov_b32_e32 v207, v208
	v_add_f32_e32 v208, 1.0, v218
	v_exp_f32_e32 v218, v211
	v_mul_f32_e32 v216, 0xbfb8aa3b, v216
	v_exp_f32_e32 v216, v216
	v_add_f32_e32 v211, 1.0, v214
	v_mul_f32_e32 v206, 0xbfb8aa3b, v206
	v_and_b32_e32 v217, 0xffff0000, v219
	v_min_f32_e32 v214, 0x49800000, v211
	v_mov_b32_e32 v211, v212
	v_add_f32_e32 v212, 1.0, v218
	v_mul_f32_e32 v218, 0xbfb8aa3b, v220
	v_exp_f32_e32 v206, v206
	v_mul_f32_e32 v215, 0xbfb8aa3b, v215
	v_exp_f32_e32 v218, v218
	v_add_f32_e32 v216, 1.0, v216
	v_mul_f32_e32 v217, 0xbfb8aa3b, v217
	v_exp_f32_e32 v215, v215
	v_min_f32_e32 v219, 0x49800000, v216
	v_exp_f32_e32 v217, v217
	v_mul_f32_e32 v204, 0xbfb8aa3b, v204
	v_add_f32_e32 v206, 1.0, v206
	v_mul_f32_e32 v205, 0xbfb8aa3b, v205
	v_add_f32_e32 v210, 1.0, v210
	v_mul_f32_e32 v209, 0xbfb8aa3b, v209
	v_add_f32_e32 v218, 1.0, v218
	v_exp_f32_e32 v204, v204
	v_min_f32_e32 v206, 0x49800000, v206
	v_exp_f32_e32 v205, v205
	v_min_f32_e32 v210, 0x49800000, v210
	v_exp_f32_e32 v209, v209
	v_mul_f32_e32 v213, 0xbfb8aa3b, v213
	v_add_f32_e32 v215, 1.0, v215
	v_rcp_f32_e32 v216, v218
	v_mov_b32_e32 v218, v219
	v_mul_f32_e32 v219, 0xbfb8aa3b, v221
	v_add_f32_e32 v217, 1.0, v217
	v_exp_f32_e32 v213, v213
	v_min_f32_e32 v215, 0x49800000, v215
	v_exp_f32_e32 v219, v219
	v_min_f32_e32 v220, 0x49800000, v217
	v_add_f32_e32 v204, 1.0, v204
	v_add_f32_e32 v205, 1.0, v205
	v_add_f32_e32 v209, 1.0, v209
	v_rcp_f32_e32 v204, v204
	v_rcp_f32_e32 v205, v205
	v_rcp_f32_e32 v208, v208
	v_rcp_f32_e32 v209, v209
	v_add_f32_e32 v213, 1.0, v213
	v_add_f32_e32 v217, 1.0, v219
	v_mov_b32_e32 v219, v220
	v_rcp_f32_e32 v212, v212
	v_rcp_f32_e32 v213, v213
	v_rcp_f32_e32 v217, v217
	v_pk_mul_f32 v[204:205], v[204:205], v[206:207]
	v_pk_mul_f32 v[206:207], v[208:209], v[210:211]
	v_pk_mul_f32 v[208:209], v[212:213], v[214:215]
	v_pk_mul_f32 v[210:211], v[216:217], v[218:219]
	v_pk_mul_f32 v[54:55], v[54:55], v[206:207]
	s_waitcnt vmcnt(11)
	v_lshlrev_b32_e32 v206, 16, v142
	v_and_b32_e32 v207, 0xffff0000, v142
	s_waitcnt vmcnt(9)
	v_lshlrev_b32_e32 v142, 16, v136
	v_pk_mul_f32 v[50:51], v[50:51], v[210:211]
	v_pk_mul_f32 v[48:49], v[48:49], v[208:209]
	v_lshlrev_b32_e32 v208, 16, v143
	v_and_b32_e32 v209, 0xffff0000, v143
	v_and_b32_e32 v143, 0xffff0000, v136
	v_lshlrev_b32_e32 v210, 16, v137
	v_and_b32_e32 v211, 0xffff0000, v137
	v_mul_f32_e32 v137, 0xbfb8aa3b, v142
	v_lshlrev_b32_e32 v212, 16, v138
	v_and_b32_e32 v213, 0xffff0000, v138
	v_exp_f32_e32 v137, v137
	v_mul_f32_e32 v138, 0xbfb8aa3b, v143
	v_exp_f32_e32 v138, v138
	v_pk_mul_f32 v[52:53], v[52:53], v[204:205]
	v_lshlrev_b32_e32 v204, 16, v140
	v_and_b32_e32 v140, 0xffff0000, v140
	v_add_f32_e32 v137, 1.0, v137
	v_mul_f32_e32 v136, 0xbfb8aa3b, v204
	v_lshlrev_b32_e32 v214, 16, v139
	v_and_b32_e32 v215, 0xffff0000, v139
	v_min_f32_e32 v137, 0x49800000, v137
	v_mul_f32_e32 v139, 0xbfb8aa3b, v140
	v_add_f32_e32 v138, 1.0, v138
	v_mul_f32_e32 v204, 0xbfb8aa3b, v212
	v_exp_f32_e32 v139, v139
	v_min_f32_e32 v140, 0x49800000, v138
	v_exp_f32_e32 v204, v204
	v_lshlrev_b32_e32 v205, 16, v141
	v_mov_b32_e32 v138, v137
	v_add_f32_e32 v137, 1.0, v139
	v_mov_b32_e32 v139, v140
	v_mul_f32_e32 v140, 0xbfb8aa3b, v205
	v_mul_f32_e32 v205, 0xbfb8aa3b, v206
	v_add_f32_e32 v204, 1.0, v204
	v_exp_f32_e32 v205, v205
	v_min_f32_e32 v206, 0x49800000, v204
	v_mul_f32_e32 v142, 0xbfb8aa3b, v210
	v_mul_f32_e32 v143, 0xbfb8aa3b, v211
	v_add_f32_e32 v204, 1.0, v205
	v_mov_b32_e32 v205, v206
	v_mul_f32_e32 v206, 0xbfb8aa3b, v207
	v_exp_f32_e32 v207, v206
	v_mul_f32_e32 v206, 0xbfb8aa3b, v213
	v_exp_f32_e32 v210, v206
	v_mov_b32_e32 v206, v205
	v_add_f32_e32 v205, 1.0, v207
	v_mul_f32_e32 v211, 0xbfb8aa3b, v215
	v_add_f32_e32 v207, 1.0, v210
	v_mul_f32_e32 v210, 0xbfb8aa3b, v214
	v_exp_f32_e32 v142, v142
	v_exp_f32_e32 v143, v143
	v_exp_f32_e32 v210, v210
	v_exp_f32_e32 v211, v211
	v_and_b32_e32 v141, 0xffff0000, v141
	v_add_f32_e32 v142, 1.0, v142
	v_mul_f32_e32 v141, 0xbfb8aa3b, v141
	v_add_f32_e32 v143, 1.0, v143
	v_mul_f32_e32 v208, 0xbfb8aa3b, v208
	v_add_f32_e32 v210, 1.0, v210
	v_mul_f32_e32 v209, 0xbfb8aa3b, v209
	v_add_f32_e32 v211, 1.0, v211
	v_exp_f32_e32 v136, v136
	v_exp_f32_e32 v140, v140
	v_min_f32_e32 v142, 0x49800000, v142
	v_exp_f32_e32 v141, v141
	v_min_f32_e32 v143, 0x49800000, v143
	v_min_f32_e32 v207, 0x49800000, v207
	v_exp_f32_e32 v208, v208
	v_min_f32_e32 v210, 0x49800000, v210
	v_exp_f32_e32 v209, v209
	v_min_f32_e32 v211, 0x49800000, v211
	v_add_f32_e32 v136, 1.0, v136
	v_add_f32_e32 v140, 1.0, v140
	v_add_f32_e32 v141, 1.0, v141
	v_add_f32_e32 v208, 1.0, v208
	v_add_f32_e32 v209, 1.0, v209
	v_rcp_f32_e32 v136, v136
	v_rcp_f32_e32 v137, v137
	v_rcp_f32_e32 v140, v140
	v_rcp_f32_e32 v141, v141
	v_rcp_f32_e32 v204, v204
	v_rcp_f32_e32 v205, v205
	v_rcp_f32_e32 v208, v208
	v_rcp_f32_e32 v209, v209
	v_pk_mul_f32 v[136:137], v[136:137], v[138:139]
	v_pk_mul_f32 v[138:139], v[140:141], v[142:143]
	v_pk_mul_f32 v[140:141], v[204:205], v[206:207]
	v_pk_mul_f32 v[142:143], v[208:209], v[210:211]
	global_load_dwordx4 v[204:207], v[190:191], off
	global_load_dwordx4 v[208:211], v[162:163], off
	v_pk_mul_f32 v[46:47], v[46:47], v[138:139]
	v_lshlrev_b32_e32 v138, 16, v134
	v_and_b32_e32 v139, 0xffff0000, v134
	s_waitcnt vmcnt(2)
	v_lshlrev_b32_e32 v134, 16, v128
	v_pk_mul_f32 v[40:41], v[40:41], v[140:141]
	v_lshlrev_b32_e32 v140, 16, v135
	v_and_b32_e32 v141, 0xffff0000, v135
	v_and_b32_e32 v135, 0xffff0000, v128
	v_mul_f32_e32 v128, 0xbfb8aa3b, v134
	v_exp_f32_e32 v128, v128
	v_pk_mul_f32 v[44:45], v[44:45], v[136:137]
	v_lshlrev_b32_e32 v136, 16, v132
	v_pk_mul_f32 v[42:43], v[42:43], v[142:143]
	v_lshlrev_b32_e32 v142, 16, v129
	v_and_b32_e32 v143, 0xffff0000, v129
	v_lshlrev_b32_e32 v212, 16, v130
	v_mul_f32_e32 v129, 0xbfb8aa3b, v136
	v_add_f32_e32 v128, 1.0, v128
	v_and_b32_e32 v213, 0xffff0000, v130
	v_exp_f32_e32 v129, v129
	v_min_f32_e32 v130, 0x49800000, v128
	v_mul_f32_e32 v136, 0xbfb8aa3b, v212
	v_exp_f32_e32 v136, v136
	v_and_b32_e32 v132, 0xffff0000, v132
	v_lshlrev_b32_e32 v137, 16, v133
	v_add_f32_e32 v128, 1.0, v129
	v_mov_b32_e32 v129, v130
	v_mul_f32_e32 v130, 0xbfb8aa3b, v135
	v_lshlrev_b32_e32 v214, 16, v131
	v_and_b32_e32 v215, 0xffff0000, v131
	v_exp_f32_e32 v131, v130
	v_mov_b32_e32 v130, v129
	v_mul_f32_e32 v129, 0xbfb8aa3b, v132
	v_mul_f32_e32 v132, 0xbfb8aa3b, v137
	v_mul_f32_e32 v137, 0xbfb8aa3b, v138
	v_add_f32_e32 v136, 1.0, v136
	v_exp_f32_e32 v137, v137
	v_min_f32_e32 v138, 0x49800000, v136
	v_mul_f32_e32 v134, 0xbfb8aa3b, v142
	v_mul_f32_e32 v135, 0xbfb8aa3b, v143
	v_add_f32_e32 v136, 1.0, v137
	v_mov_b32_e32 v137, v138
	v_mul_f32_e32 v138, 0xbfb8aa3b, v139
	v_exp_f32_e32 v139, v138
	v_mul_f32_e32 v138, 0xbfb8aa3b, v213
	v_exp_f32_e32 v142, v138
	v_mov_b32_e32 v138, v137
	v_add_f32_e32 v137, 1.0, v139
	v_mul_f32_e32 v143, 0xbfb8aa3b, v215
	v_add_f32_e32 v139, 1.0, v142
	v_mul_f32_e32 v142, 0xbfb8aa3b, v214
	v_exp_f32_e32 v134, v134
	v_exp_f32_e32 v135, v135
	v_exp_f32_e32 v142, v142
	v_exp_f32_e32 v143, v143
	v_and_b32_e32 v133, 0xffff0000, v133
	v_add_f32_e32 v131, 1.0, v131
	v_add_f32_e32 v134, 1.0, v134
	v_mul_f32_e32 v133, 0xbfb8aa3b, v133
	v_add_f32_e32 v135, 1.0, v135
	v_mul_f32_e32 v140, 0xbfb8aa3b, v140
	v_add_f32_e32 v142, 1.0, v142
	v_mul_f32_e32 v141, 0xbfb8aa3b, v141
	v_add_f32_e32 v143, 1.0, v143
	v_exp_f32_e32 v129, v129
	v_min_f32_e32 v131, 0x49800000, v131
	v_exp_f32_e32 v132, v132
	v_min_f32_e32 v134, 0x49800000, v134
	v_exp_f32_e32 v133, v133
	v_min_f32_e32 v135, 0x49800000, v135
	v_min_f32_e32 v139, 0x49800000, v139
	v_exp_f32_e32 v140, v140
	v_min_f32_e32 v142, 0x49800000, v142
	v_exp_f32_e32 v141, v141
	v_min_f32_e32 v143, 0x49800000, v143
	v_add_f32_e32 v129, 1.0, v129
	v_add_f32_e32 v132, 1.0, v132
	v_add_f32_e32 v133, 1.0, v133
	v_add_f32_e32 v140, 1.0, v140
	v_add_f32_e32 v141, 1.0, v141
	v_rcp_f32_e32 v128, v128
	v_rcp_f32_e32 v129, v129
	v_rcp_f32_e32 v132, v132
	v_rcp_f32_e32 v133, v133
	v_rcp_f32_e32 v136, v136
	v_rcp_f32_e32 v137, v137
	v_rcp_f32_e32 v140, v140
	v_rcp_f32_e32 v141, v141
	v_pk_mul_f32 v[128:129], v[128:129], v[130:131]
	v_pk_mul_f32 v[130:131], v[132:133], v[134:135]
	v_pk_mul_f32 v[132:133], v[136:137], v[138:139]
	v_pk_mul_f32 v[134:135], v[140:141], v[142:143]
	v_pk_mul_f32 v[38:39], v[38:39], v[130:131]
	v_pk_mul_f32 v[36:37], v[36:37], v[128:129]
	v_pk_mul_f32 v[34:35], v[34:35], v[134:135]
	v_pk_mul_f32 v[32:33], v[32:33], v[132:133]
	global_load_dwordx4 v[128:131], v[164:165], off offset:256
	s_waitcnt vmcnt(2)
	v_lshlrev_b32_e32 v220, 16, v204
	v_and_b32_e32 v221, 0xffff0000, v204
	s_waitcnt vmcnt(1)
	v_lshlrev_b32_e32 v204, 16, v208
	v_mul_f32_e32 v204, 0xbfb8aa3b, v204
	v_exp_f32_e32 v204, v204
	v_lshlrev_b32_e32 v222, 16, v205
	v_and_b32_e32 v223, 0xffff0000, v205
	v_lshlrev_b32_e32 v224, 16, v206
	v_and_b32_e32 v225, 0xffff0000, v206
	v_and_b32_e32 v205, 0xffff0000, v208
	v_mul_f32_e32 v206, 0xbfb8aa3b, v220
	v_exp_f32_e32 v206, v206
	v_add_f32_e32 v204, 1.0, v204
	v_mul_f32_e32 v205, 0xbfb8aa3b, v205
	v_min_f32_e32 v208, 0x49800000, v204
	v_exp_f32_e32 v205, v205
	v_add_f32_e32 v206, 1.0, v206
	v_rcp_f32_e32 v204, v206
	v_mov_b32_e32 v206, v208
	v_mul_f32_e32 v208, 0xbfb8aa3b, v221
	v_add_f32_e32 v205, 1.0, v205
	v_lshlrev_b32_e32 v228, 16, v210
	v_and_b32_e32 v229, 0xffff0000, v210
	v_exp_f32_e32 v208, v208
	v_min_f32_e32 v210, 0x49800000, v205
	v_lshlrev_b32_e32 v226, 16, v207
	v_and_b32_e32 v227, 0xffff0000, v207
	v_lshlrev_b32_e32 v207, 16, v209
	v_add_f32_e32 v205, 1.0, v208
	v_mov_b32_e32 v208, v210
	v_mul_f32_e32 v210, 0xbfb8aa3b, v222
	v_mul_f32_e32 v207, 0xbfb8aa3b, v207
	v_lshlrev_b32_e32 v230, 16, v211
	v_and_b32_e32 v231, 0xffff0000, v211
	v_exp_f32_e32 v210, v210
	v_exp_f32_e32 v211, v207
	v_and_b32_e32 v209, 0xffff0000, v209
	v_mov_b32_e32 v207, v208
	v_add_f32_e32 v208, 1.0, v210
	v_add_f32_e32 v210, 1.0, v211
	v_mul_f32_e32 v211, 0xbfb8aa3b, v223
	v_mul_f32_e32 v209, 0xbfb8aa3b, v209
	v_exp_f32_e32 v211, v211
	v_exp_f32_e32 v209, v209
	v_mul_f32_e32 v221, 0xbfb8aa3b, v224
	v_exp_f32_e32 v221, v221
	v_add_f32_e32 v211, 1.0, v211
	v_add_f32_e32 v209, 1.0, v209
	v_min_f32_e32 v220, 0x49800000, v209
	v_rcp_f32_e32 v209, v211
	v_mul_f32_e32 v211, 0xbfb8aa3b, v228
	v_exp_f32_e32 v211, v211
	v_min_f32_e32 v210, 0x49800000, v210
	v_add_f32_e32 v211, 1.0, v211
	v_min_f32_e32 v222, 0x49800000, v211
	v_mov_b32_e32 v211, v220
	v_add_f32_e32 v220, 1.0, v221
	v_mov_b32_e32 v221, v222
	v_mul_f32_e32 v222, 0xbfb8aa3b, v225
	v_exp_f32_e32 v223, v222
	v_mul_f32_e32 v222, 0xbfb8aa3b, v229
	v_exp_f32_e32 v224, v222
	v_mov_b32_e32 v222, v221
	v_add_f32_e32 v221, 1.0, v223
	v_mul_f32_e32 v225, 0xbfb8aa3b, v230
	v_add_f32_e32 v223, 1.0, v224
	v_min_f32_e32 v223, 0x49800000, v223
	v_mul_f32_e32 v224, 0xbfb8aa3b, v226
	v_exp_f32_e32 v225, v225
	v_mul_f32_e32 v226, 0xbfb8aa3b, v231
	v_exp_f32_e32 v226, v226
	v_rcp_f32_e32 v205, v205
	v_rcp_f32_e32 v208, v208
	v_rcp_f32_e32 v220, v220
	v_rcp_f32_e32 v221, v221
	v_add_f32_e32 v225, 1.0, v225
	v_min_f32_e32 v225, 0x49800000, v225
	v_mul_f32_e32 v227, 0xbfb8aa3b, v227
	v_add_f32_e32 v226, 1.0, v226
	v_exp_f32_e32 v224, v224
	v_exp_f32_e32 v227, v227
	v_min_f32_e32 v228, 0x49800000, v226
	v_pk_mul_f32 v[204:205], v[204:205], v[206:207]
	v_pk_mul_f32 v[206:207], v[208:209], v[210:211]
	v_pk_mul_f32 v[208:209], v[220:221], v[222:223]
	v_pk_mul_f32 v[24:25], v[24:25], v[208:209]
	s_waitcnt vmcnt(7)
	v_and_b32_e32 v208, 0xffff0000, v236
	v_mul_f32_e32 v208, 0xbfb8aa3b, v208
	v_add_f32_e32 v224, 1.0, v224
	v_mov_b32_e32 v226, v225
	v_add_f32_e32 v225, 1.0, v227
	v_mov_b32_e32 v227, v228
	v_exp_f32_e32 v208, v208
	v_rcp_f32_e32 v224, v224
	v_rcp_f32_e32 v225, v225
	v_pk_mul_f32 v[28:29], v[28:29], v[204:205]
	v_lshlrev_b32_e32 v204, 16, v232
	v_and_b32_e32 v205, 0xffff0000, v232
	v_and_b32_e32 v232, 0xffff0000, v237
	v_mul_f32_e32 v232, 0xbfb8aa3b, v232
	v_pk_mul_f32 v[30:31], v[30:31], v[206:207]
	v_lshlrev_b32_e32 v207, 16, v233
	v_add_f32_e32 v208, 1.0, v208
	v_exp_f32_e32 v232, v232
	v_pk_mul_f32 v[210:211], v[224:225], v[226:227]
	v_min_f32_e32 v208, 0x49800000, v208
	v_mul_f32_e32 v207, 0xbfb8aa3b, v207
	v_pk_mul_f32 v[26:27], v[26:27], v[210:211]
	v_and_b32_e32 v209, 0xffff0000, v233
	v_lshlrev_b32_e32 v211, 16, v234
	v_and_b32_e32 v233, 0xffff0000, v234
	v_lshlrev_b32_e32 v220, 16, v235
	v_and_b32_e32 v221, 0xffff0000, v235
	v_lshlrev_b32_e32 v234, 16, v238
	v_and_b32_e32 v235, 0xffff0000, v238
	v_exp_f32_e32 v238, v207
	v_lshlrev_b32_e32 v210, 16, v237
	v_add_f32_e32 v232, 1.0, v232
	v_mul_f32_e32 v234, 0xbfb8aa3b, v234
	v_lshlrev_b32_e32 v206, 16, v236
	v_lshlrev_b32_e32 v236, 16, v239
	v_mul_f32_e32 v207, 0xbfb8aa3b, v210
	v_min_f32_e32 v232, 0x49800000, v232
	v_exp_f32_e32 v234, v234
	v_mul_f32_e32 v211, 0xbfb8aa3b, v211
	v_exp_f32_e32 v210, v207
	v_mov_b32_e32 v207, v208
	v_add_f32_e32 v208, 1.0, v238
	v_exp_f32_e32 v238, v211
	v_mul_f32_e32 v236, 0xbfb8aa3b, v236
	v_exp_f32_e32 v236, v236
	v_add_f32_e32 v211, 1.0, v234
	v_mul_f32_e32 v206, 0xbfb8aa3b, v206
	v_and_b32_e32 v237, 0xffff0000, v239
	v_min_f32_e32 v234, 0x49800000, v211
	v_mov_b32_e32 v211, v232
	v_add_f32_e32 v232, 1.0, v238
	v_mul_f32_e32 v238, 0xbfb8aa3b, v220
	v_exp_f32_e32 v206, v206
	v_mul_f32_e32 v235, 0xbfb8aa3b, v235
	v_exp_f32_e32 v238, v238
	v_add_f32_e32 v236, 1.0, v236
	v_mul_f32_e32 v237, 0xbfb8aa3b, v237
	v_exp_f32_e32 v235, v235
	v_min_f32_e32 v239, 0x49800000, v236
	v_exp_f32_e32 v237, v237
	v_mul_f32_e32 v204, 0xbfb8aa3b, v204
	v_add_f32_e32 v206, 1.0, v206
	v_mul_f32_e32 v205, 0xbfb8aa3b, v205
	v_add_f32_e32 v210, 1.0, v210
	v_mul_f32_e32 v209, 0xbfb8aa3b, v209
	v_add_f32_e32 v238, 1.0, v238
	v_exp_f32_e32 v204, v204
	v_min_f32_e32 v206, 0x49800000, v206
	v_exp_f32_e32 v205, v205
	v_min_f32_e32 v210, 0x49800000, v210
	v_exp_f32_e32 v209, v209
	v_mul_f32_e32 v233, 0xbfb8aa3b, v233
	v_add_f32_e32 v235, 1.0, v235
	v_rcp_f32_e32 v236, v238
	v_mov_b32_e32 v238, v239
	v_mul_f32_e32 v239, 0xbfb8aa3b, v221
	v_add_f32_e32 v237, 1.0, v237
	v_exp_f32_e32 v233, v233
	v_min_f32_e32 v235, 0x49800000, v235
	v_exp_f32_e32 v239, v239
	v_min_f32_e32 v220, 0x49800000, v237
	v_add_f32_e32 v204, 1.0, v204
	v_add_f32_e32 v205, 1.0, v205
	v_add_f32_e32 v209, 1.0, v209
	v_rcp_f32_e32 v204, v204
	v_rcp_f32_e32 v205, v205
	v_rcp_f32_e32 v208, v208
	v_rcp_f32_e32 v209, v209
	v_add_f32_e32 v233, 1.0, v233
	v_add_f32_e32 v237, 1.0, v239
	v_mov_b32_e32 v239, v220
	v_rcp_f32_e32 v232, v232
	v_rcp_f32_e32 v233, v233
	v_rcp_f32_e32 v237, v237
	v_pk_mul_f32 v[204:205], v[204:205], v[206:207]
	v_pk_mul_f32 v[206:207], v[208:209], v[210:211]
	v_pk_mul_f32 v[208:209], v[232:233], v[234:235]
	v_pk_mul_f32 v[210:211], v[236:237], v[238:239]
	v_pk_mul_f32 v[22:23], v[22:23], v[206:207]
	s_waitcnt vmcnt(6)
	v_lshlrev_b32_e32 v206, 16, v242
	v_and_b32_e32 v207, 0xffff0000, v242
	s_waitcnt vmcnt(4)
	v_lshlrev_b32_e32 v242, 16, v248
	v_pk_mul_f32 v[18:19], v[18:19], v[210:211]
	v_pk_mul_f32 v[16:17], v[16:17], v[208:209]
	v_lshlrev_b32_e32 v208, 16, v243
	v_and_b32_e32 v209, 0xffff0000, v243
	v_and_b32_e32 v243, 0xffff0000, v248
	v_lshlrev_b32_e32 v210, 16, v249
	v_and_b32_e32 v211, 0xffff0000, v249
	v_mul_f32_e32 v249, 0xbfb8aa3b, v242
	v_lshlrev_b32_e32 v232, 16, v250
	v_and_b32_e32 v233, 0xffff0000, v250
	v_exp_f32_e32 v249, v249
	v_mul_f32_e32 v250, 0xbfb8aa3b, v243
	v_exp_f32_e32 v250, v250
	v_pk_mul_f32 v[20:21], v[20:21], v[204:205]
	v_lshlrev_b32_e32 v204, 16, v240
	v_and_b32_e32 v240, 0xffff0000, v240
	v_add_f32_e32 v249, 1.0, v249
	v_mul_f32_e32 v248, 0xbfb8aa3b, v204
	v_lshlrev_b32_e32 v234, 16, v251
	v_and_b32_e32 v235, 0xffff0000, v251
	v_min_f32_e32 v249, 0x49800000, v249
	v_mul_f32_e32 v251, 0xbfb8aa3b, v240
	v_add_f32_e32 v250, 1.0, v250
	v_mul_f32_e32 v204, 0xbfb8aa3b, v232
	v_exp_f32_e32 v251, v251
	v_min_f32_e32 v240, 0x49800000, v250
	v_exp_f32_e32 v204, v204
	v_lshlrev_b32_e32 v205, 16, v241
	v_mov_b32_e32 v250, v249
	v_add_f32_e32 v249, 1.0, v251
	v_mov_b32_e32 v251, v240
	v_mul_f32_e32 v240, 0xbfb8aa3b, v205
	v_mul_f32_e32 v205, 0xbfb8aa3b, v206
	v_add_f32_e32 v204, 1.0, v204
	v_exp_f32_e32 v205, v205
	v_min_f32_e32 v206, 0x49800000, v204
	v_mul_f32_e32 v242, 0xbfb8aa3b, v210
	v_mul_f32_e32 v243, 0xbfb8aa3b, v211
	v_add_f32_e32 v204, 1.0, v205
	v_mov_b32_e32 v205, v206
	v_mul_f32_e32 v206, 0xbfb8aa3b, v207
	v_exp_f32_e32 v207, v206
	v_mul_f32_e32 v206, 0xbfb8aa3b, v233
	v_exp_f32_e32 v210, v206
	v_exp_f32_e32 v242, v242
	v_exp_f32_e32 v243, v243
	v_mov_b32_e32 v206, v205
	v_add_f32_e32 v205, 1.0, v207
	v_add_f32_e32 v207, 1.0, v210
	v_mul_f32_e32 v210, 0xbfb8aa3b, v234
	v_mul_f32_e32 v211, 0xbfb8aa3b, v235
	v_exp_f32_e32 v210, v210
	v_exp_f32_e32 v211, v211
	v_and_b32_e32 v241, 0xffff0000, v241
	v_add_f32_e32 v242, 1.0, v242
	v_mul_f32_e32 v241, 0xbfb8aa3b, v241
	v_add_f32_e32 v243, 1.0, v243
	v_exp_f32_e32 v248, v248
	v_exp_f32_e32 v240, v240
	v_min_f32_e32 v242, 0x49800000, v242
	v_exp_f32_e32 v241, v241
	v_min_f32_e32 v243, 0x49800000, v243
	v_mul_f32_e32 v208, 0xbfb8aa3b, v208
	v_add_f32_e32 v210, 1.0, v210
	v_mul_f32_e32 v209, 0xbfb8aa3b, v209
	v_add_f32_e32 v211, 1.0, v211
	v_min_f32_e32 v207, 0x49800000, v207
	v_exp_f32_e32 v208, v208
	v_min_f32_e32 v210, 0x49800000, v210
	v_exp_f32_e32 v209, v209
	v_min_f32_e32 v211, 0x49800000, v211
	v_add_f32_e32 v248, 1.0, v248
	v_add_f32_e32 v240, 1.0, v240
	v_add_f32_e32 v241, 1.0, v241
	v_rcp_f32_e32 v248, v248
	v_rcp_f32_e32 v249, v249
	v_rcp_f32_e32 v240, v240
	v_rcp_f32_e32 v241, v241
	v_add_f32_e32 v208, 1.0, v208
	v_add_f32_e32 v209, 1.0, v209
	v_rcp_f32_e32 v204, v204
	v_rcp_f32_e32 v205, v205
	v_rcp_f32_e32 v208, v208
	v_rcp_f32_e32 v209, v209
	v_pk_mul_f32 v[248:249], v[248:249], v[250:251]
	v_pk_mul_f32 v[250:251], v[240:241], v[242:243]
	v_pk_mul_f32 v[240:241], v[204:205], v[206:207]
	v_pk_mul_f32 v[242:243], v[208:209], v[210:211]
	v_pk_mul_f32 v[14:15], v[14:15], v[250:251]
	v_lshlrev_b32_e32 v250, 16, v246
	v_and_b32_e32 v251, 0xffff0000, v246
	s_waitcnt vmcnt(0)
	v_lshlrev_b32_e32 v246, 16, v128
	v_pk_mul_f32 v[10:11], v[10:11], v[242:243]
	v_pk_mul_f32 v[8:9], v[8:9], v[240:241]
	v_lshlrev_b32_e32 v240, 16, v247
	v_and_b32_e32 v241, 0xffff0000, v247
	v_and_b32_e32 v247, 0xffff0000, v128
	v_lshlrev_b32_e32 v242, 16, v129
	v_and_b32_e32 v243, 0xffff0000, v129
	v_mul_f32_e32 v129, 0xbfb8aa3b, v246
	v_lshlrev_b32_e32 v204, 16, v130
	v_and_b32_e32 v205, 0xffff0000, v130
	v_exp_f32_e32 v129, v129
	v_mul_f32_e32 v130, 0xbfb8aa3b, v247
	v_exp_f32_e32 v130, v130
	v_pk_mul_f32 v[12:13], v[12:13], v[248:249]
	v_lshlrev_b32_e32 v248, 16, v244
	v_and_b32_e32 v244, 0xffff0000, v244
	v_add_f32_e32 v129, 1.0, v129
	v_mul_f32_e32 v128, 0xbfb8aa3b, v248
	v_lshlrev_b32_e32 v206, 16, v131
	v_and_b32_e32 v207, 0xffff0000, v131
	v_min_f32_e32 v129, 0x49800000, v129
	v_mul_f32_e32 v131, 0xbfb8aa3b, v244
	v_add_f32_e32 v130, 1.0, v130
	v_mul_f32_e32 v248, 0xbfb8aa3b, v204
	v_exp_f32_e32 v131, v131
	v_min_f32_e32 v244, 0x49800000, v130
	v_exp_f32_e32 v248, v248
	v_lshlrev_b32_e32 v249, 16, v245
	v_mov_b32_e32 v130, v129
	v_add_f32_e32 v129, 1.0, v131
	v_mov_b32_e32 v131, v244
	v_mul_f32_e32 v244, 0xbfb8aa3b, v249
	v_mul_f32_e32 v249, 0xbfb8aa3b, v250
	v_add_f32_e32 v248, 1.0, v248
	v_exp_f32_e32 v249, v249
	v_min_f32_e32 v250, 0x49800000, v248
	v_mul_f32_e32 v246, 0xbfb8aa3b, v242
	v_mul_f32_e32 v247, 0xbfb8aa3b, v243
	v_add_f32_e32 v248, 1.0, v249
	v_mov_b32_e32 v249, v250
	v_mul_f32_e32 v250, 0xbfb8aa3b, v251
	v_exp_f32_e32 v251, v250
	v_mul_f32_e32 v250, 0xbfb8aa3b, v205
	v_exp_f32_e32 v242, v250
	v_mov_b32_e32 v250, v249
	v_add_f32_e32 v249, 1.0, v251
	v_mul_f32_e32 v243, 0xbfb8aa3b, v207
	v_add_f32_e32 v251, 1.0, v242
	v_mul_f32_e32 v242, 0xbfb8aa3b, v206
	v_exp_f32_e32 v246, v246
	v_exp_f32_e32 v247, v247
	v_exp_f32_e32 v242, v242
	v_exp_f32_e32 v243, v243
	v_and_b32_e32 v245, 0xffff0000, v245
	v_add_f32_e32 v246, 1.0, v246
	v_mul_f32_e32 v245, 0xbfb8aa3b, v245
	v_add_f32_e32 v247, 1.0, v247
	v_mul_f32_e32 v240, 0xbfb8aa3b, v240
	v_add_f32_e32 v242, 1.0, v242
	v_mul_f32_e32 v241, 0xbfb8aa3b, v241
	v_add_f32_e32 v243, 1.0, v243
	v_exp_f32_e32 v128, v128
	v_exp_f32_e32 v244, v244
	v_min_f32_e32 v246, 0x49800000, v246
	v_exp_f32_e32 v245, v245
	v_min_f32_e32 v247, 0x49800000, v247
	v_min_f32_e32 v251, 0x49800000, v251
	v_exp_f32_e32 v240, v240
	v_min_f32_e32 v242, 0x49800000, v242
	v_exp_f32_e32 v241, v241
	v_min_f32_e32 v243, 0x49800000, v243
	v_add_f32_e32 v128, 1.0, v128
	v_add_f32_e32 v244, 1.0, v244
	v_add_f32_e32 v245, 1.0, v245
	v_add_f32_e32 v240, 1.0, v240
	v_add_f32_e32 v241, 1.0, v241
	v_rcp_f32_e32 v128, v128
	v_rcp_f32_e32 v129, v129
	v_rcp_f32_e32 v244, v244
	v_rcp_f32_e32 v245, v245
	v_rcp_f32_e32 v248, v248
	v_rcp_f32_e32 v249, v249
	v_rcp_f32_e32 v240, v240
	v_rcp_f32_e32 v241, v241
	v_pk_mul_f32 v[128:129], v[128:129], v[130:131]
	v_pk_mul_f32 v[130:131], v[244:245], v[246:247]
	v_pk_mul_f32 v[244:245], v[248:249], v[250:251]
	v_pk_mul_f32 v[246:247], v[240:241], v[242:243]
	v_pk_mul_f32 v[2:3], v[2:3], v[130:131]
	v_pk_mul_f32 v[0:1], v[0:1], v[128:129]
	v_pk_mul_f32 v[6:7], v[6:7], v[246:247]
	v_pk_mul_f32 v[4:5], v[4:5], v[244:245]

.LBB0_873:
	global_load_dwordx4 v[178:181], v[144:145], off
	global_load_dwordx4 v[182:185], v[144:145], off offset:256
	global_load_dwordx4 v[186:189], v[146:147], off
	s_nop 0
	global_load_dwordx4 v[144:147], v[146:147], off offset:256
	s_nop 0
	global_load_dwordx4 v[140:143], v[174:175], off
	global_load_dwordx4 v[136:139], v[174:175], off offset:256
	global_load_dwordx4 v[132:135], v[176:177], off
	global_load_dwordx4 v[128:131], v[176:177], off offset:256
	global_load_dwordx4 v[224:227], v[158:159], off
	global_load_dwordx4 v[228:231], v[158:159], off offset:256
	global_load_dwordx4 v[232:235], v[160:161], off
	global_load_dwordx4 v[220:223], v[160:161], off offset:256
	global_load_dwordx4 v[216:219], v[162:163], off
	global_load_dwordx4 v[212:215], v[162:163], off offset:256
	global_load_dwordx4 v[208:211], v[164:165], off
	global_load_dwordx4 v[204:207], v[164:165], off offset:256
	s_and_b64 vcc, exec, s[20:21]
	s_cbranch_vccz .LBB0_875
	s_barrier
.LBB0_875:
	v_lshlrev_b64 v[172:173], 12, v[172:173]
	v_lshl_add_u64 v[172:173], s[16:17], 0, v[172:173]
	v_lshl_add_u64 v[172:173], v[172:173], 0, v[148:149]
	s_and_b64 vcc, exec, s[4:5]
	s_mov_b64 s[4:5], -1
	s_waitcnt vmcnt(15)
	v_lshlrev_b32_e32 v174, 16, v178
	v_and_b32_e32 v175, 0xffff0000, v178
	v_lshlrev_b32_e32 v176, 16, v179
	v_and_b32_e32 v177, 0xffff0000, v179
	v_lshlrev_b32_e32 v178, 16, v180
	v_and_b32_e32 v179, 0xffff0000, v180
	v_lshlrev_b32_e32 v180, 16, v181
	v_and_b32_e32 v181, 0xffff0000, v181
	v_mul_f32_e32 v181, 0xbfb8aa3b, v181
	v_mul_f32_e32 v174, 0xbfb8aa3b, v174
	v_mul_f32_e32 v175, 0xbfb8aa3b, v175
	v_mul_f32_e32 v176, 0xbfb8aa3b, v176
	v_mul_f32_e32 v177, 0xbfb8aa3b, v177
	v_mul_f32_e32 v178, 0xbfb8aa3b, v178
	v_mul_f32_e32 v179, 0xbfb8aa3b, v179
	v_mul_f32_e32 v180, 0xbfb8aa3b, v180
	v_exp_f32_e32 v181, v181
	v_exp_f32_e32 v174, v174
	v_exp_f32_e32 v175, v175
	v_exp_f32_e32 v176, v176
	v_exp_f32_e32 v177, v177
	v_exp_f32_e32 v178, v178
	v_exp_f32_e32 v179, v179
	v_exp_f32_e32 v180, v180
	v_add_f32_e32 v181, 1.0, v181
	v_add_f32_e32 v174, 1.0, v174
	v_add_f32_e32 v175, 1.0, v175
	v_add_f32_e32 v176, 1.0, v176
	v_add_f32_e32 v177, 1.0, v177
	v_add_f32_e32 v178, 1.0, v178
	v_add_f32_e32 v179, 1.0, v179
	v_add_f32_e32 v180, 1.0, v180
	v_rcp_f32_e32 v181, v181
	v_rcp_f32_e32 v174, v174
	v_rcp_f32_e32 v175, v175
	v_rcp_f32_e32 v176, v176
	v_rcp_f32_e32 v177, v177
	v_rcp_f32_e32 v178, v178
	v_rcp_f32_e32 v179, v179
	v_rcp_f32_e32 v180, v180
	v_max_f32_e32 v181, 0x35800000, v181
	s_waitcnt vmcnt(14)
	v_lshlrev_b32_e32 v190, 16, v182
	v_and_b32_e32 v182, 0xffff0000, v182
	v_max_f32_e32 v174, 0x35800000, v174
	v_max_f32_e32 v175, 0x35800000, v175
	v_max_f32_e32 v176, 0x35800000, v176
	v_max_f32_e32 v177, 0x35800000, v177
	v_max_f32_e32 v178, 0x35800000, v178
	v_max_f32_e32 v179, 0x35800000, v179
	v_max_f32_e32 v180, 0x35800000, v180
	v_mul_f32_e32 v123, v123, v181
	v_lshlrev_b32_e32 v191, 16, v183
	v_and_b32_e32 v183, 0xffff0000, v183
	v_lshlrev_b32_e32 v192, 16, v184
	v_and_b32_e32 v184, 0xffff0000, v184
	v_mul_f32_e32 v190, 0xbfb8aa3b, v190
	v_mul_f32_e32 v182, 0xbfb8aa3b, v182
	v_mul_f32_e32 v124, v124, v174
	v_mul_f32_e32 v125, v125, v175
	v_mul_f32_e32 v126, v126, v176
	v_mul_f32_e32 v127, v127, v177
	v_mul_f32_e32 v174, v120, v178
	v_mul_f32_e32 v175, v121, v179
	v_mul_f32_e32 v176, v122, v180
	v_cvt_pk_bf16_f32 v120, v124, v125
	v_cvt_pk_bf16_f32 v121, v126, v127
	v_cvt_pk_bf16_f32 v122, v174, v175
	v_cvt_pk_bf16_f32 v123, v176, v123
	v_lshlrev_b32_e32 v193, 16, v185
	v_and_b32_e32 v185, 0xffff0000, v185
	v_mul_f32_e32 v191, 0xbfb8aa3b, v191
	v_mul_f32_e32 v183, 0xbfb8aa3b, v183
	v_exp_f32_e32 v190, v190
	v_exp_f32_e32 v182, v182
	global_store_dwordx4 v[172:173], v[120:123], off
	v_mul_f32_e32 v124, 0xbfb8aa3b, v184
	v_exp_f32_e32 v191, v191
	v_mul_f32_e32 v123, 0xbfb8aa3b, v192
	v_exp_f32_e32 v183, v183
	v_exp_f32_e32 v123, v123
	v_exp_f32_e32 v124, v124
	v_mul_f32_e32 v125, 0xbfb8aa3b, v193
	v_mul_f32_e32 v126, 0xbfb8aa3b, v185
	v_exp_f32_e32 v125, v125
	v_exp_f32_e32 v126, v126
	v_add_f32_e32 v190, 1.0, v190
	v_add_f32_e32 v182, 1.0, v182
	v_add_f32_e32 v191, 1.0, v191
	v_rcp_f32_e32 v190, v190
	v_rcp_f32_e32 v182, v182
	v_add_f32_e32 v122, 1.0, v183
	v_add_f32_e32 v123, 1.0, v123
	v_add_f32_e32 v124, 1.0, v124
	v_rcp_f32_e32 v191, v191
	v_rcp_f32_e32 v122, v122
	v_rcp_f32_e32 v123, v123
	v_rcp_f32_e32 v124, v124
	v_add_f32_e32 v125, 1.0, v125
	v_add_f32_e32 v126, 1.0, v126
	v_rcp_f32_e32 v125, v125
	v_rcp_f32_e32 v126, v126
	v_max_f32_e32 v190, 0x35800000, v190
	v_max_f32_e32 v120, 0x35800000, v182
	v_max_f32_e32 v121, 0x35800000, v191
	v_max_f32_e32 v122, 0x35800000, v122
	v_max_f32_e32 v123, 0x35800000, v123
	v_max_f32_e32 v124, 0x35800000, v124
	v_mul_f32_e32 v116, v116, v190
	v_mul_f32_e32 v117, v117, v120
	v_max_f32_e32 v125, 0x35800000, v125
	v_max_f32_e32 v126, 0x35800000, v126
	v_cvt_pk_bf16_f32 v116, v116, v117
	v_mul_f32_e32 v117, v118, v121
	v_mul_f32_e32 v118, v119, v122
	v_mul_f32_e32 v112, v112, v123
	v_mul_f32_e32 v113, v113, v124
	v_cvt_pk_bf16_f32 v117, v117, v118
	v_cvt_pk_bf16_f32 v118, v112, v113
	v_mul_f32_e32 v112, v114, v125
	v_mul_f32_e32 v113, v115, v126
	v_cvt_pk_bf16_f32 v119, v112, v113
	s_waitcnt vmcnt(14)
	v_lshlrev_b32_e32 v114, 16, v186
	v_and_b32_e32 v115, 0xffff0000, v186
	global_store_dwordx4 v[172:173], v[116:119], off offset:256
	v_mul_f32_e32 v114, 0xbfb8aa3b, v114
	v_mul_f32_e32 v115, 0xbfb8aa3b, v115
	v_lshlrev_b32_e32 v116, 16, v187
	v_and_b32_e32 v117, 0xffff0000, v187
	v_lshlrev_b32_e32 v118, 16, v188
	v_and_b32_e32 v119, 0xffff0000, v188
	v_exp_f32_e32 v114, v114
	v_lshlrev_b32_e32 v120, 16, v189
	v_and_b32_e32 v121, 0xffff0000, v189
	v_exp_f32_e32 v115, v115
	v_mul_f32_e32 v116, 0xbfb8aa3b, v116
	v_mul_f32_e32 v117, 0xbfb8aa3b, v117
	v_mul_f32_e32 v118, 0xbfb8aa3b, v118
	v_mul_f32_e32 v119, 0xbfb8aa3b, v119
	v_exp_f32_e32 v116, v116
	v_exp_f32_e32 v117, v117
	v_exp_f32_e32 v118, v118
	v_exp_f32_e32 v119, v119
	v_mul_f32_e32 v120, 0xbfb8aa3b, v120
	v_mul_f32_e32 v121, 0xbfb8aa3b, v121
	v_exp_f32_e32 v120, v120
	v_exp_f32_e32 v121, v121
	v_add_f32_e32 v114, 1.0, v114
	v_add_f32_e32 v115, 1.0, v115
	v_rcp_f32_e32 v114, v114
	v_rcp_f32_e32 v115, v115
	v_add_f32_e32 v116, 1.0, v116
	v_add_f32_e32 v117, 1.0, v117
	v_add_f32_e32 v118, 1.0, v118
	v_add_f32_e32 v119, 1.0, v119
	v_rcp_f32_e32 v116, v116
	v_rcp_f32_e32 v117, v117
	v_rcp_f32_e32 v118, v118
	v_rcp_f32_e32 v119, v119
	v_add_f32_e32 v120, 1.0, v120
	v_add_f32_e32 v121, 1.0, v121
	v_rcp_f32_e32 v120, v120
	v_rcp_f32_e32 v121, v121
	v_max_f32_e32 v114, 0x35800000, v114
	v_max_f32_e32 v115, 0x35800000, v115
	v_max_f32_e32 v116, 0x35800000, v116
	v_max_f32_e32 v117, 0x35800000, v117
	v_max_f32_e32 v118, 0x35800000, v118
	v_max_f32_e32 v119, 0x35800000, v119
	v_mul_f32_e32 v108, v108, v114
	v_mul_f32_e32 v109, v109, v115
	v_max_f32_e32 v120, 0x35800000, v120
	v_max_f32_e32 v121, 0x35800000, v121
	v_cvt_pk_bf16_f32 v108, v108, v109
	v_mul_f32_e32 v109, v110, v116
	v_mul_f32_e32 v110, v111, v117
	v_mul_f32_e32 v104, v104, v118
	v_mul_f32_e32 v105, v105, v119
	v_lshlrev_b64 v[112:113], 12, v[170:171]
	v_cvt_pk_bf16_f32 v109, v109, v110
	v_cvt_pk_bf16_f32 v110, v104, v105
	v_mul_f32_e32 v104, v106, v120
	v_mul_f32_e32 v105, v107, v121
	v_cvt_pk_bf16_f32 v111, v104, v105
	v_lshl_add_u64 v[104:105], s[16:17], 0, v[112:113]
	v_lshl_add_u64 v[104:105], v[104:105], 0, v[148:149]
	s_waitcnt vmcnt(14)
	v_lshlrev_b32_e32 v106, 16, v144
	v_and_b32_e32 v107, 0xffff0000, v144
	global_store_dwordx4 v[104:105], v[108:111], off
	v_mul_f32_e32 v106, 0xbfb8aa3b, v106
	v_mul_f32_e32 v107, 0xbfb8aa3b, v107
	v_lshlrev_b32_e32 v108, 16, v145
	v_and_b32_e32 v109, 0xffff0000, v145
	v_lshlrev_b32_e32 v110, 16, v146
	v_and_b32_e32 v111, 0xffff0000, v146
	v_exp_f32_e32 v106, v106
	v_lshlrev_b32_e32 v112, 16, v147
	v_and_b32_e32 v113, 0xffff0000, v147
	v_exp_f32_e32 v107, v107
	v_mul_f32_e32 v108, 0xbfb8aa3b, v108
	v_mul_f32_e32 v109, 0xbfb8aa3b, v109
	v_mul_f32_e32 v110, 0xbfb8aa3b, v110
	v_mul_f32_e32 v111, 0xbfb8aa3b, v111
	v_exp_f32_e32 v108, v108
	v_exp_f32_e32 v109, v109
	v_exp_f32_e32 v110, v110
	v_exp_f32_e32 v111, v111
	v_mul_f32_e32 v112, 0xbfb8aa3b, v112
	v_mul_f32_e32 v113, 0xbfb8aa3b, v113
	v_exp_f32_e32 v112, v112
	v_exp_f32_e32 v113, v113
	v_add_f32_e32 v106, 1.0, v106
	v_add_f32_e32 v107, 1.0, v107
	v_rcp_f32_e32 v106, v106
	v_rcp_f32_e32 v107, v107
	v_add_f32_e32 v108, 1.0, v108
	v_add_f32_e32 v109, 1.0, v109
	v_add_f32_e32 v110, 1.0, v110
	v_add_f32_e32 v111, 1.0, v111
	v_rcp_f32_e32 v108, v108
	v_rcp_f32_e32 v109, v109
	v_rcp_f32_e32 v110, v110
	v_rcp_f32_e32 v111, v111
	v_add_f32_e32 v112, 1.0, v112
	v_add_f32_e32 v113, 1.0, v113
	v_rcp_f32_e32 v112, v112
	v_rcp_f32_e32 v113, v113
	v_max_f32_e32 v106, 0x35800000, v106
	v_max_f32_e32 v107, 0x35800000, v107
	v_max_f32_e32 v108, 0x35800000, v108
	v_max_f32_e32 v109, 0x35800000, v109
	v_max_f32_e32 v110, 0x35800000, v110
	v_max_f32_e32 v111, 0x35800000, v111
	v_mul_f32_e32 v100, v100, v106
	v_mul_f32_e32 v101, v101, v107
	v_max_f32_e32 v112, 0x35800000, v112
	v_max_f32_e32 v113, 0x35800000, v113
	v_cvt_pk_bf16_f32 v100, v100, v101
	v_mul_f32_e32 v101, v102, v108
	v_mul_f32_e32 v102, v103, v109
	v_mul_f32_e32 v96, v96, v110
	v_mul_f32_e32 v97, v97, v111
	v_cvt_pk_bf16_f32 v101, v101, v102
	v_cvt_pk_bf16_f32 v102, v96, v97
	v_mul_f32_e32 v96, v98, v112
	v_mul_f32_e32 v97, v99, v113
	v_cvt_pk_bf16_f32 v103, v96, v97
	s_waitcnt vmcnt(14)
	v_lshlrev_b32_e32 v98, 16, v140
	v_and_b32_e32 v99, 0xffff0000, v140
	global_store_dwordx4 v[104:105], v[100:103], off offset:256
	v_mul_f32_e32 v98, 0xbfb8aa3b, v98
	v_mul_f32_e32 v99, 0xbfb8aa3b, v99
	v_lshlrev_b32_e32 v100, 16, v141
	v_and_b32_e32 v101, 0xffff0000, v141
	v_lshlrev_b32_e32 v102, 16, v142
	v_and_b32_e32 v103, 0xffff0000, v142
	v_exp_f32_e32 v98, v98
	v_lshlrev_b32_e32 v104, 16, v143
	v_and_b32_e32 v105, 0xffff0000, v143
	v_exp_f32_e32 v99, v99
	v_mul_f32_e32 v100, 0xbfb8aa3b, v100
	v_mul_f32_e32 v101, 0xbfb8aa3b, v101
	v_mul_f32_e32 v102, 0xbfb8aa3b, v102
	v_mul_f32_e32 v103, 0xbfb8aa3b, v103
	v_exp_f32_e32 v100, v100
	v_exp_f32_e32 v101, v101
	v_exp_f32_e32 v102, v102
	v_exp_f32_e32 v103, v103
	v_mul_f32_e32 v104, 0xbfb8aa3b, v104
	v_mul_f32_e32 v105, 0xbfb8aa3b, v105
	v_exp_f32_e32 v104, v104
	v_exp_f32_e32 v105, v105
	v_add_f32_e32 v98, 1.0, v98
	v_add_f32_e32 v99, 1.0, v99
	v_rcp_f32_e32 v98, v98
	v_rcp_f32_e32 v99, v99
	v_add_f32_e32 v100, 1.0, v100
	v_add_f32_e32 v101, 1.0, v101
	v_add_f32_e32 v102, 1.0, v102
	v_add_f32_e32 v103, 1.0, v103
	v_rcp_f32_e32 v100, v100
	v_rcp_f32_e32 v101, v101
	v_rcp_f32_e32 v102, v102
	v_rcp_f32_e32 v103, v103
	v_add_f32_e32 v104, 1.0, v104
	v_add_f32_e32 v105, 1.0, v105
	v_rcp_f32_e32 v104, v104
	v_rcp_f32_e32 v105, v105
	v_max_f32_e32 v98, 0x35800000, v98
	v_max_f32_e32 v99, 0x35800000, v99
	v_max_f32_e32 v100, 0x35800000, v100
	v_max_f32_e32 v101, 0x35800000, v101
	v_max_f32_e32 v102, 0x35800000, v102
	v_max_f32_e32 v103, 0x35800000, v103
	v_mul_f32_e32 v92, v92, v98
	v_mul_f32_e32 v93, v93, v99
	v_max_f32_e32 v104, 0x35800000, v104
	v_max_f32_e32 v105, 0x35800000, v105
	v_cvt_pk_bf16_f32 v92, v92, v93
	v_mul_f32_e32 v93, v94, v100
	v_mul_f32_e32 v94, v95, v101
	v_mul_f32_e32 v88, v88, v102
	v_mul_f32_e32 v89, v89, v103
	v_lshlrev_b64 v[96:97], 12, v[168:169]
	v_cvt_pk_bf16_f32 v93, v93, v94
	v_cvt_pk_bf16_f32 v94, v88, v89
	v_mul_f32_e32 v88, v90, v104
	v_mul_f32_e32 v89, v91, v105
	v_cvt_pk_bf16_f32 v95, v88, v89
	v_lshl_add_u64 v[88:89], s[16:17], 0, v[96:97]
	v_lshl_add_u64 v[88:89], v[88:89], 0, v[148:149]
	s_waitcnt vmcnt(14)
	v_lshlrev_b32_e32 v90, 16, v136
	v_and_b32_e32 v91, 0xffff0000, v136
	global_store_dwordx4 v[88:89], v[92:95], off
	v_mul_f32_e32 v90, 0xbfb8aa3b, v90
	v_mul_f32_e32 v91, 0xbfb8aa3b, v91
	v_lshlrev_b32_e32 v92, 16, v137
	v_and_b32_e32 v93, 0xffff0000, v137
	v_lshlrev_b32_e32 v94, 16, v138
	v_and_b32_e32 v95, 0xffff0000, v138
	v_exp_f32_e32 v90, v90
	v_lshlrev_b32_e32 v96, 16, v139
	v_and_b32_e32 v97, 0xffff0000, v139
	v_exp_f32_e32 v91, v91
	v_mul_f32_e32 v92, 0xbfb8aa3b, v92
	v_mul_f32_e32 v93, 0xbfb8aa3b, v93
	v_mul_f32_e32 v94, 0xbfb8aa3b, v94
	v_mul_f32_e32 v95, 0xbfb8aa3b, v95
	v_exp_f32_e32 v92, v92
	v_exp_f32_e32 v93, v93
	v_exp_f32_e32 v94, v94
	v_exp_f32_e32 v95, v95
	v_mul_f32_e32 v96, 0xbfb8aa3b, v96
	v_mul_f32_e32 v97, 0xbfb8aa3b, v97
	v_exp_f32_e32 v96, v96
	v_exp_f32_e32 v97, v97
	v_add_f32_e32 v90, 1.0, v90
	v_add_f32_e32 v91, 1.0, v91
	v_rcp_f32_e32 v90, v90
	v_rcp_f32_e32 v91, v91
	v_add_f32_e32 v92, 1.0, v92
	v_add_f32_e32 v93, 1.0, v93
	v_add_f32_e32 v94, 1.0, v94
	v_add_f32_e32 v95, 1.0, v95
	v_rcp_f32_e32 v92, v92
	v_rcp_f32_e32 v93, v93
	v_rcp_f32_e32 v94, v94
	v_rcp_f32_e32 v95, v95
	v_add_f32_e32 v96, 1.0, v96
	v_add_f32_e32 v97, 1.0, v97
	v_rcp_f32_e32 v96, v96
	v_rcp_f32_e32 v97, v97
	v_max_f32_e32 v90, 0x35800000, v90
	v_max_f32_e32 v91, 0x35800000, v91
	v_max_f32_e32 v92, 0x35800000, v92
	v_max_f32_e32 v93, 0x35800000, v93
	v_max_f32_e32 v94, 0x35800000, v94
	v_max_f32_e32 v95, 0x35800000, v95
	v_mul_f32_e32 v84, v84, v90
	v_mul_f32_e32 v85, v85, v91
	v_max_f32_e32 v96, 0x35800000, v96
	v_max_f32_e32 v97, 0x35800000, v97
	v_cvt_pk_bf16_f32 v84, v84, v85
	v_mul_f32_e32 v85, v86, v92
	v_mul_f32_e32 v86, v87, v93
	v_mul_f32_e32 v80, v80, v94
	v_mul_f32_e32 v81, v81, v95
	v_cvt_pk_bf16_f32 v85, v85, v86
	v_cvt_pk_bf16_f32 v86, v80, v81
	v_mul_f32_e32 v80, v82, v96
	v_mul_f32_e32 v81, v83, v97
	v_cvt_pk_bf16_f32 v87, v80, v81
	s_waitcnt vmcnt(14)
	v_lshlrev_b32_e32 v82, 16, v132
	v_and_b32_e32 v83, 0xffff0000, v132
	global_store_dwordx4 v[88:89], v[84:87], off offset:256
	v_mul_f32_e32 v82, 0xbfb8aa3b, v82
	v_mul_f32_e32 v83, 0xbfb8aa3b, v83
	v_lshlrev_b32_e32 v84, 16, v133
	v_and_b32_e32 v85, 0xffff0000, v133
	v_lshlrev_b32_e32 v86, 16, v134
	v_and_b32_e32 v87, 0xffff0000, v134
	v_exp_f32_e32 v82, v82
	v_lshlrev_b32_e32 v88, 16, v135
	v_and_b32_e32 v89, 0xffff0000, v135
	v_exp_f32_e32 v83, v83
	v_mul_f32_e32 v84, 0xbfb8aa3b, v84
	v_mul_f32_e32 v85, 0xbfb8aa3b, v85
	v_mul_f32_e32 v86, 0xbfb8aa3b, v86
	v_mul_f32_e32 v87, 0xbfb8aa3b, v87
	v_exp_f32_e32 v84, v84
	v_exp_f32_e32 v85, v85
	v_exp_f32_e32 v86, v86
	v_exp_f32_e32 v87, v87
	v_mul_f32_e32 v88, 0xbfb8aa3b, v88
	v_mul_f32_e32 v89, 0xbfb8aa3b, v89
	v_exp_f32_e32 v88, v88
	v_exp_f32_e32 v89, v89
	v_add_f32_e32 v82, 1.0, v82
	v_add_f32_e32 v83, 1.0, v83
	v_rcp_f32_e32 v82, v82
	v_rcp_f32_e32 v83, v83
	v_add_f32_e32 v84, 1.0, v84
	v_add_f32_e32 v85, 1.0, v85
	v_add_f32_e32 v86, 1.0, v86
	v_add_f32_e32 v87, 1.0, v87
	v_rcp_f32_e32 v84, v84
	v_rcp_f32_e32 v85, v85
	v_rcp_f32_e32 v86, v86
	v_rcp_f32_e32 v87, v87
	v_add_f32_e32 v88, 1.0, v88
	v_add_f32_e32 v89, 1.0, v89
	v_rcp_f32_e32 v88, v88
	v_rcp_f32_e32 v89, v89
	v_max_f32_e32 v82, 0x35800000, v82
	v_max_f32_e32 v83, 0x35800000, v83
	v_max_f32_e32 v84, 0x35800000, v84
	v_max_f32_e32 v85, 0x35800000, v85
	v_max_f32_e32 v86, 0x35800000, v86
	v_max_f32_e32 v87, 0x35800000, v87
	v_mul_f32_e32 v76, v76, v82
	v_mul_f32_e32 v77, v77, v83
	v_max_f32_e32 v88, 0x35800000, v88
	v_max_f32_e32 v89, 0x35800000, v89
	v_cvt_pk_bf16_f32 v76, v76, v77
	v_mul_f32_e32 v77, v78, v84
	v_mul_f32_e32 v78, v79, v85
	v_mul_f32_e32 v72, v72, v86
	v_mul_f32_e32 v73, v73, v87
	v_lshlrev_b64 v[80:81], 12, v[166:167]
	v_cvt_pk_bf16_f32 v77, v77, v78
	v_cvt_pk_bf16_f32 v78, v72, v73
	v_mul_f32_e32 v72, v74, v88
	v_mul_f32_e32 v73, v75, v89
	v_cvt_pk_bf16_f32 v79, v72, v73
	v_lshl_add_u64 v[72:73], s[16:17], 0, v[80:81]
	v_lshl_add_u64 v[72:73], v[72:73], 0, v[148:149]
	s_waitcnt vmcnt(14)
	v_lshlrev_b32_e32 v74, 16, v128
	v_and_b32_e32 v75, 0xffff0000, v128
	global_store_dwordx4 v[72:73], v[76:79], off
	v_mul_f32_e32 v74, 0xbfb8aa3b, v74
	v_mul_f32_e32 v75, 0xbfb8aa3b, v75
	v_lshlrev_b32_e32 v76, 16, v129
	v_and_b32_e32 v77, 0xffff0000, v129
	v_lshlrev_b32_e32 v78, 16, v130
	v_and_b32_e32 v79, 0xffff0000, v130
	v_exp_f32_e32 v74, v74
	v_lshlrev_b32_e32 v80, 16, v131
	v_and_b32_e32 v81, 0xffff0000, v131
	v_exp_f32_e32 v75, v75
	v_mul_f32_e32 v76, 0xbfb8aa3b, v76
	v_mul_f32_e32 v77, 0xbfb8aa3b, v77
	v_mul_f32_e32 v78, 0xbfb8aa3b, v78
	v_mul_f32_e32 v79, 0xbfb8aa3b, v79
	v_exp_f32_e32 v76, v76
	v_exp_f32_e32 v77, v77
	v_exp_f32_e32 v78, v78
	v_exp_f32_e32 v79, v79
	v_mul_f32_e32 v80, 0xbfb8aa3b, v80
	v_mul_f32_e32 v81, 0xbfb8aa3b, v81
	v_exp_f32_e32 v80, v80
	v_exp_f32_e32 v81, v81
	v_add_f32_e32 v74, 1.0, v74
	v_add_f32_e32 v75, 1.0, v75
	v_rcp_f32_e32 v74, v74
	v_rcp_f32_e32 v75, v75
	v_add_f32_e32 v76, 1.0, v76
	v_add_f32_e32 v77, 1.0, v77
	v_add_f32_e32 v78, 1.0, v78
	v_add_f32_e32 v79, 1.0, v79
	v_rcp_f32_e32 v76, v76
	v_rcp_f32_e32 v77, v77
	v_rcp_f32_e32 v78, v78
	v_rcp_f32_e32 v79, v79
	v_add_f32_e32 v80, 1.0, v80
	v_add_f32_e32 v81, 1.0, v81
	v_rcp_f32_e32 v80, v80
	v_rcp_f32_e32 v81, v81
	v_max_f32_e32 v74, 0x35800000, v74
	v_max_f32_e32 v75, 0x35800000, v75
	v_max_f32_e32 v76, 0x35800000, v76
	v_max_f32_e32 v77, 0x35800000, v77
	v_max_f32_e32 v78, 0x35800000, v78
	v_max_f32_e32 v79, 0x35800000, v79
	v_mul_f32_e32 v68, v68, v74
	v_mul_f32_e32 v69, v69, v75
	v_max_f32_e32 v80, 0x35800000, v80
	v_max_f32_e32 v81, 0x35800000, v81
	v_cvt_pk_bf16_f32 v68, v68, v69
	v_mul_f32_e32 v69, v70, v76
	v_mul_f32_e32 v70, v71, v77
	v_mul_f32_e32 v64, v64, v78
	v_mul_f32_e32 v65, v65, v79
	v_cvt_pk_bf16_f32 v69, v69, v70
	v_cvt_pk_bf16_f32 v70, v64, v65
	v_mul_f32_e32 v64, v66, v80
	v_mul_f32_e32 v65, v67, v81
	v_cvt_pk_bf16_f32 v71, v64, v65
	v_lshlrev_b64 v[96:97], 12, v[156:157]
	global_store_dwordx4 v[72:73], v[68:71], off offset:256
	s_nop 0
	s_waitcnt vmcnt(15)
	v_lshlrev_b32_e32 v98, 16, v224
	v_and_b32_e32 v224, 0xffff0000, v224
	v_lshlrev_b32_e32 v99, 16, v225
	v_and_b32_e32 v225, 0xffff0000, v225
	v_lshlrev_b32_e32 v100, 16, v226
	v_mul_f32_e32 v98, 0xbfb8aa3b, v98
	v_and_b32_e32 v226, 0xffff0000, v226
	v_mul_f32_e32 v224, 0xbfb8aa3b, v224
	v_exp_f32_e32 v98, v98
	v_lshlrev_b32_e32 v101, 16, v227
	v_and_b32_e32 v227, 0xffff0000, v227
	v_exp_f32_e32 v224, v224
	v_mul_f32_e32 v99, 0xbfb8aa3b, v99
	v_mul_f32_e32 v225, 0xbfb8aa3b, v225
	v_mul_f32_e32 v100, 0xbfb8aa3b, v100
	v_mul_f32_e32 v226, 0xbfb8aa3b, v226
	v_exp_f32_e32 v99, v99
	v_exp_f32_e32 v225, v225
	v_exp_f32_e32 v100, v100
	v_exp_f32_e32 v226, v226
	v_mul_f32_e32 v101, 0xbfb8aa3b, v101
	v_mul_f32_e32 v227, 0xbfb8aa3b, v227
	v_exp_f32_e32 v101, v101
	v_exp_f32_e32 v227, v227
	v_add_f32_e32 v98, 1.0, v98
	v_add_f32_e32 v224, 1.0, v224
	v_rcp_f32_e32 v98, v98
	v_rcp_f32_e32 v224, v224
	v_add_f32_e32 v99, 1.0, v99
	v_add_f32_e32 v225, 1.0, v225
	v_add_f32_e32 v100, 1.0, v100
	v_add_f32_e32 v226, 1.0, v226
	v_rcp_f32_e32 v99, v99
	v_rcp_f32_e32 v225, v225
	v_rcp_f32_e32 v100, v100
	v_rcp_f32_e32 v226, v226
	v_add_f32_e32 v101, 1.0, v101
	v_add_f32_e32 v227, 1.0, v227
	v_rcp_f32_e32 v101, v101
	v_rcp_f32_e32 v227, v227
	v_max_f32_e32 v98, 0x35800000, v98
	v_max_f32_e32 v224, 0x35800000, v224
	v_max_f32_e32 v99, 0x35800000, v99
	v_max_f32_e32 v225, 0x35800000, v225
	v_max_f32_e32 v100, 0x35800000, v100
	v_max_f32_e32 v226, 0x35800000, v226
	v_mul_f32_e32 v60, v60, v98
	v_mul_f32_e32 v61, v61, v224
	v_max_f32_e32 v101, 0x35800000, v101
	v_max_f32_e32 v227, 0x35800000, v227
	v_cvt_pk_bf16_f32 v60, v60, v61
	v_mul_f32_e32 v61, v62, v99
	v_mul_f32_e32 v62, v63, v225
	v_mul_f32_e32 v56, v56, v100
	v_mul_f32_e32 v57, v57, v226
	v_cvt_pk_bf16_f32 v61, v61, v62
	v_cvt_pk_bf16_f32 v62, v56, v57
	v_mul_f32_e32 v56, v58, v101
	v_mul_f32_e32 v57, v59, v227
	v_cvt_pk_bf16_f32 v63, v56, v57
	v_lshl_add_u64 v[56:57], s[16:17], 0, v[96:97]
	v_lshl_add_u64 v[56:57], v[56:57], 0, v[148:149]
	s_waitcnt vmcnt(14)
	v_lshlrev_b32_e32 v58, 16, v228
	v_and_b32_e32 v59, 0xffff0000, v228
	global_store_dwordx4 v[56:57], v[60:63], off
	v_mul_f32_e32 v58, 0xbfb8aa3b, v58
	v_mul_f32_e32 v59, 0xbfb8aa3b, v59
	v_lshlrev_b32_e32 v60, 16, v229
	v_and_b32_e32 v61, 0xffff0000, v229
	v_lshlrev_b32_e32 v62, 16, v230
	v_and_b32_e32 v63, 0xffff0000, v230
	v_exp_f32_e32 v58, v58
	v_lshlrev_b32_e32 v224, 16, v231
	v_and_b32_e32 v225, 0xffff0000, v231
	v_exp_f32_e32 v59, v59
	v_mul_f32_e32 v60, 0xbfb8aa3b, v60
	v_mul_f32_e32 v61, 0xbfb8aa3b, v61
	v_mul_f32_e32 v62, 0xbfb8aa3b, v62
	v_mul_f32_e32 v63, 0xbfb8aa3b, v63
	v_exp_f32_e32 v60, v60
	v_exp_f32_e32 v61, v61
	v_exp_f32_e32 v62, v62
	v_exp_f32_e32 v63, v63
	v_mul_f32_e32 v224, 0xbfb8aa3b, v224
	v_mul_f32_e32 v225, 0xbfb8aa3b, v225
	v_exp_f32_e32 v224, v224
	v_exp_f32_e32 v225, v225
	v_add_f32_e32 v58, 1.0, v58
	v_add_f32_e32 v59, 1.0, v59
	v_rcp_f32_e32 v58, v58
	v_rcp_f32_e32 v59, v59
	v_add_f32_e32 v60, 1.0, v60
	v_add_f32_e32 v61, 1.0, v61
	v_add_f32_e32 v62, 1.0, v62
	v_add_f32_e32 v63, 1.0, v63
	v_rcp_f32_e32 v60, v60
	v_rcp_f32_e32 v61, v61
	v_rcp_f32_e32 v62, v62
	v_rcp_f32_e32 v63, v63
	v_add_f32_e32 v224, 1.0, v224
	v_add_f32_e32 v225, 1.0, v225
	v_rcp_f32_e32 v224, v224
	v_rcp_f32_e32 v225, v225
	v_max_f32_e32 v58, 0x35800000, v58
	v_max_f32_e32 v59, 0x35800000, v59
	v_max_f32_e32 v60, 0x35800000, v60
	v_max_f32_e32 v61, 0x35800000, v61
	v_max_f32_e32 v62, 0x35800000, v62
	v_max_f32_e32 v63, 0x35800000, v63
	v_mul_f32_e32 v52, v52, v58
	v_mul_f32_e32 v53, v53, v59
	v_max_f32_e32 v224, 0x35800000, v224
	v_max_f32_e32 v225, 0x35800000, v225
	v_cvt_pk_bf16_f32 v52, v52, v53
	v_mul_f32_e32 v53, v54, v60
	v_mul_f32_e32 v54, v55, v61
	v_mul_f32_e32 v48, v48, v62
	v_mul_f32_e32 v49, v49, v63
	v_cvt_pk_bf16_f32 v53, v53, v54
	v_cvt_pk_bf16_f32 v54, v48, v49
	v_mul_f32_e32 v48, v50, v224
	v_mul_f32_e32 v49, v51, v225
	v_cvt_pk_bf16_f32 v55, v48, v49
	s_waitcnt vmcnt(14)
	v_lshlrev_b32_e32 v50, 16, v232
	v_and_b32_e32 v51, 0xffff0000, v232
	global_store_dwordx4 v[56:57], v[52:55], off offset:256
	v_mul_f32_e32 v50, 0xbfb8aa3b, v50
	v_mul_f32_e32 v51, 0xbfb8aa3b, v51
	v_lshlrev_b32_e32 v52, 16, v233
	v_and_b32_e32 v53, 0xffff0000, v233
	v_lshlrev_b32_e32 v54, 16, v234
	v_and_b32_e32 v55, 0xffff0000, v234
	v_exp_f32_e32 v50, v50
	v_lshlrev_b32_e32 v56, 16, v235
	v_and_b32_e32 v57, 0xffff0000, v235
	v_exp_f32_e32 v51, v51
	v_mul_f32_e32 v52, 0xbfb8aa3b, v52
	v_mul_f32_e32 v53, 0xbfb8aa3b, v53
	v_mul_f32_e32 v54, 0xbfb8aa3b, v54
	v_mul_f32_e32 v55, 0xbfb8aa3b, v55
	v_exp_f32_e32 v52, v52
	v_exp_f32_e32 v53, v53
	v_exp_f32_e32 v54, v54
	v_exp_f32_e32 v55, v55
	v_mul_f32_e32 v56, 0xbfb8aa3b, v56
	v_mul_f32_e32 v57, 0xbfb8aa3b, v57
	v_exp_f32_e32 v56, v56
	v_exp_f32_e32 v57, v57
	v_add_f32_e32 v50, 1.0, v50
	v_add_f32_e32 v51, 1.0, v51
	v_rcp_f32_e32 v50, v50
	v_rcp_f32_e32 v51, v51
	v_add_f32_e32 v52, 1.0, v52
	v_add_f32_e32 v53, 1.0, v53
	v_add_f32_e32 v54, 1.0, v54
	v_add_f32_e32 v55, 1.0, v55
	v_rcp_f32_e32 v52, v52
	v_rcp_f32_e32 v53, v53
	v_rcp_f32_e32 v54, v54
	v_rcp_f32_e32 v55, v55
	v_add_f32_e32 v56, 1.0, v56
	v_add_f32_e32 v57, 1.0, v57
	v_rcp_f32_e32 v56, v56
	v_rcp_f32_e32 v57, v57
	v_max_f32_e32 v50, 0x35800000, v50
	v_max_f32_e32 v51, 0x35800000, v51
	v_max_f32_e32 v52, 0x35800000, v52
	v_max_f32_e32 v53, 0x35800000, v53
	v_max_f32_e32 v54, 0x35800000, v54
	v_max_f32_e32 v55, 0x35800000, v55
	v_mul_f32_e32 v44, v44, v50
	v_mul_f32_e32 v45, v45, v51
	v_max_f32_e32 v56, 0x35800000, v56
	v_max_f32_e32 v57, 0x35800000, v57
	v_cvt_pk_bf16_f32 v44, v44, v45
	v_mul_f32_e32 v45, v46, v52
	v_mul_f32_e32 v46, v47, v53
	v_mul_f32_e32 v40, v40, v54
	v_mul_f32_e32 v41, v41, v55
	v_lshlrev_b64 v[48:49], 12, v[154:155]
	v_cvt_pk_bf16_f32 v45, v45, v46
	v_cvt_pk_bf16_f32 v46, v40, v41
	v_mul_f32_e32 v40, v42, v56
	v_mul_f32_e32 v41, v43, v57
	v_cvt_pk_bf16_f32 v47, v40, v41
	v_lshl_add_u64 v[40:41], s[16:17], 0, v[48:49]
	v_lshl_add_u64 v[40:41], v[40:41], 0, v[148:149]
	s_waitcnt vmcnt(14)
	v_lshlrev_b32_e32 v42, 16, v220
	v_and_b32_e32 v43, 0xffff0000, v220
	global_store_dwordx4 v[40:41], v[44:47], off
	v_mul_f32_e32 v42, 0xbfb8aa3b, v42
	v_mul_f32_e32 v43, 0xbfb8aa3b, v43
	v_lshlrev_b32_e32 v44, 16, v221
	v_and_b32_e32 v45, 0xffff0000, v221
	v_lshlrev_b32_e32 v46, 16, v222
	v_and_b32_e32 v47, 0xffff0000, v222
	v_exp_f32_e32 v42, v42
	v_lshlrev_b32_e32 v48, 16, v223
	v_and_b32_e32 v49, 0xffff0000, v223
	v_exp_f32_e32 v43, v43
	v_mul_f32_e32 v44, 0xbfb8aa3b, v44
	v_mul_f32_e32 v45, 0xbfb8aa3b, v45
	v_mul_f32_e32 v46, 0xbfb8aa3b, v46
	v_mul_f32_e32 v47, 0xbfb8aa3b, v47
	v_exp_f32_e32 v44, v44
	v_exp_f32_e32 v45, v45
	v_exp_f32_e32 v46, v46
	v_exp_f32_e32 v47, v47
	v_mul_f32_e32 v48, 0xbfb8aa3b, v48
	v_mul_f32_e32 v49, 0xbfb8aa3b, v49
	v_exp_f32_e32 v48, v48
	v_exp_f32_e32 v49, v49
	v_add_f32_e32 v42, 1.0, v42
	v_add_f32_e32 v43, 1.0, v43
	v_rcp_f32_e32 v42, v42
	v_rcp_f32_e32 v43, v43
	v_add_f32_e32 v44, 1.0, v44
	v_add_f32_e32 v45, 1.0, v45
	v_add_f32_e32 v46, 1.0, v46
	v_add_f32_e32 v47, 1.0, v47
	v_rcp_f32_e32 v44, v44
	v_rcp_f32_e32 v45, v45
	v_rcp_f32_e32 v46, v46
	v_rcp_f32_e32 v47, v47
	v_add_f32_e32 v48, 1.0, v48
	v_add_f32_e32 v49, 1.0, v49
	v_rcp_f32_e32 v48, v48
	v_rcp_f32_e32 v49, v49
	v_max_f32_e32 v42, 0x35800000, v42
	v_max_f32_e32 v43, 0x35800000, v43
	v_max_f32_e32 v44, 0x35800000, v44
	v_max_f32_e32 v45, 0x35800000, v45
	v_max_f32_e32 v46, 0x35800000, v46
	v_max_f32_e32 v47, 0x35800000, v47
	v_mul_f32_e32 v36, v36, v42
	v_mul_f32_e32 v37, v37, v43
	v_max_f32_e32 v48, 0x35800000, v48
	v_max_f32_e32 v49, 0x35800000, v49
	v_cvt_pk_bf16_f32 v36, v36, v37
	v_mul_f32_e32 v37, v38, v44
	v_mul_f32_e32 v38, v39, v45
	v_mul_f32_e32 v32, v32, v46
	v_mul_f32_e32 v33, v33, v47
	v_cvt_pk_bf16_f32 v37, v37, v38
	v_cvt_pk_bf16_f32 v38, v32, v33
	v_mul_f32_e32 v32, v34, v48
	v_mul_f32_e32 v33, v35, v49
	v_cvt_pk_bf16_f32 v39, v32, v33
	s_waitcnt vmcnt(14)
	v_lshlrev_b32_e32 v34, 16, v216
	v_and_b32_e32 v35, 0xffff0000, v216
	global_store_dwordx4 v[40:41], v[36:39], off offset:256
	v_mul_f32_e32 v34, 0xbfb8aa3b, v34
	v_mul_f32_e32 v35, 0xbfb8aa3b, v35
	v_lshlrev_b32_e32 v36, 16, v217
	v_and_b32_e32 v37, 0xffff0000, v217
	v_lshlrev_b32_e32 v38, 16, v218
	v_and_b32_e32 v39, 0xffff0000, v218
	v_exp_f32_e32 v34, v34
	v_lshlrev_b32_e32 v40, 16, v219
	v_and_b32_e32 v41, 0xffff0000, v219
	v_exp_f32_e32 v35, v35
	v_mul_f32_e32 v36, 0xbfb8aa3b, v36
	v_mul_f32_e32 v37, 0xbfb8aa3b, v37
	v_mul_f32_e32 v38, 0xbfb8aa3b, v38
	v_mul_f32_e32 v39, 0xbfb8aa3b, v39
	v_exp_f32_e32 v36, v36
	v_exp_f32_e32 v37, v37
	v_exp_f32_e32 v38, v38
	v_exp_f32_e32 v39, v39
	v_mul_f32_e32 v40, 0xbfb8aa3b, v40
	v_mul_f32_e32 v41, 0xbfb8aa3b, v41
	v_exp_f32_e32 v40, v40
	v_exp_f32_e32 v41, v41
	v_add_f32_e32 v34, 1.0, v34
	v_add_f32_e32 v35, 1.0, v35
	v_rcp_f32_e32 v34, v34
	v_rcp_f32_e32 v35, v35
	v_add_f32_e32 v36, 1.0, v36
	v_add_f32_e32 v37, 1.0, v37
	v_add_f32_e32 v38, 1.0, v38
	v_add_f32_e32 v39, 1.0, v39
	v_rcp_f32_e32 v36, v36
	v_rcp_f32_e32 v37, v37
	v_rcp_f32_e32 v38, v38
	v_rcp_f32_e32 v39, v39
	v_add_f32_e32 v40, 1.0, v40
	v_add_f32_e32 v41, 1.0, v41
	v_rcp_f32_e32 v40, v40
	v_rcp_f32_e32 v41, v41
	v_max_f32_e32 v34, 0x35800000, v34
	v_max_f32_e32 v35, 0x35800000, v35
	v_max_f32_e32 v36, 0x35800000, v36
	v_max_f32_e32 v37, 0x35800000, v37
	v_max_f32_e32 v38, 0x35800000, v38
	v_max_f32_e32 v39, 0x35800000, v39
	v_mul_f32_e32 v28, v28, v34
	v_mul_f32_e32 v29, v29, v35
	v_max_f32_e32 v40, 0x35800000, v40
	v_max_f32_e32 v41, 0x35800000, v41
	v_cvt_pk_bf16_f32 v28, v28, v29
	v_mul_f32_e32 v29, v30, v36
	v_mul_f32_e32 v30, v31, v37
	v_mul_f32_e32 v24, v24, v38
	v_mul_f32_e32 v25, v25, v39
	v_lshlrev_b64 v[32:33], 12, v[152:153]
	v_cvt_pk_bf16_f32 v29, v29, v30
	v_cvt_pk_bf16_f32 v30, v24, v25
	v_mul_f32_e32 v24, v26, v40
	v_mul_f32_e32 v25, v27, v41
	v_cvt_pk_bf16_f32 v31, v24, v25
	v_lshl_add_u64 v[24:25], s[16:17], 0, v[32:33]
	v_lshl_add_u64 v[24:25], v[24:25], 0, v[148:149]
	s_waitcnt vmcnt(14)
	v_lshlrev_b32_e32 v26, 16, v212
	v_and_b32_e32 v27, 0xffff0000, v212
	global_store_dwordx4 v[24:25], v[28:31], off
	v_mul_f32_e32 v26, 0xbfb8aa3b, v26
	v_mul_f32_e32 v27, 0xbfb8aa3b, v27
	v_lshlrev_b32_e32 v28, 16, v213
	v_and_b32_e32 v29, 0xffff0000, v213
	v_lshlrev_b32_e32 v30, 16, v214
	v_and_b32_e32 v31, 0xffff0000, v214
	v_exp_f32_e32 v26, v26
	v_lshlrev_b32_e32 v32, 16, v215
	v_and_b32_e32 v33, 0xffff0000, v215
	v_exp_f32_e32 v27, v27
	v_mul_f32_e32 v28, 0xbfb8aa3b, v28
	v_mul_f32_e32 v29, 0xbfb8aa3b, v29
	v_mul_f32_e32 v30, 0xbfb8aa3b, v30
	v_mul_f32_e32 v31, 0xbfb8aa3b, v31
	v_exp_f32_e32 v28, v28
	v_exp_f32_e32 v29, v29
	v_exp_f32_e32 v30, v30
	v_exp_f32_e32 v31, v31
	v_mul_f32_e32 v32, 0xbfb8aa3b, v32
	v_mul_f32_e32 v33, 0xbfb8aa3b, v33
	v_exp_f32_e32 v32, v32
	v_exp_f32_e32 v33, v33
	v_add_f32_e32 v26, 1.0, v26
	v_add_f32_e32 v27, 1.0, v27
	v_rcp_f32_e32 v26, v26
	v_rcp_f32_e32 v27, v27
	v_add_f32_e32 v28, 1.0, v28
	v_add_f32_e32 v29, 1.0, v29
	v_add_f32_e32 v30, 1.0, v30
	v_add_f32_e32 v31, 1.0, v31
	v_rcp_f32_e32 v28, v28
	v_rcp_f32_e32 v29, v29
	v_rcp_f32_e32 v30, v30
	v_rcp_f32_e32 v31, v31
	v_add_f32_e32 v32, 1.0, v32
	v_add_f32_e32 v33, 1.0, v33
	v_rcp_f32_e32 v32, v32
	v_rcp_f32_e32 v33, v33
	v_max_f32_e32 v26, 0x35800000, v26
	v_max_f32_e32 v27, 0x35800000, v27
	v_max_f32_e32 v28, 0x35800000, v28
	v_max_f32_e32 v29, 0x35800000, v29
	v_max_f32_e32 v30, 0x35800000, v30
	v_max_f32_e32 v31, 0x35800000, v31
	v_mul_f32_e32 v20, v20, v26
	v_mul_f32_e32 v21, v21, v27
	v_max_f32_e32 v32, 0x35800000, v32
	v_max_f32_e32 v33, 0x35800000, v33
	v_cvt_pk_bf16_f32 v20, v20, v21
	v_mul_f32_e32 v21, v22, v28
	v_mul_f32_e32 v22, v23, v29
	v_mul_f32_e32 v16, v16, v30
	v_mul_f32_e32 v17, v17, v31
	v_cvt_pk_bf16_f32 v21, v21, v22
	v_cvt_pk_bf16_f32 v22, v16, v17
	v_mul_f32_e32 v16, v18, v32
	v_mul_f32_e32 v17, v19, v33
	v_cvt_pk_bf16_f32 v23, v16, v17
	s_waitcnt vmcnt(14)
	v_lshlrev_b32_e32 v18, 16, v208
	v_and_b32_e32 v19, 0xffff0000, v208
	global_store_dwordx4 v[24:25], v[20:23], off offset:256
	v_mul_f32_e32 v18, 0xbfb8aa3b, v18
	v_mul_f32_e32 v19, 0xbfb8aa3b, v19
	v_lshlrev_b32_e32 v20, 16, v209
	v_and_b32_e32 v21, 0xffff0000, v209
	v_lshlrev_b32_e32 v22, 16, v210
	v_and_b32_e32 v23, 0xffff0000, v210
	v_exp_f32_e32 v18, v18
	v_lshlrev_b32_e32 v24, 16, v211
	v_and_b32_e32 v25, 0xffff0000, v211
	v_exp_f32_e32 v19, v19
	v_mul_f32_e32 v20, 0xbfb8aa3b, v20
	v_mul_f32_e32 v21, 0xbfb8aa3b, v21
	v_mul_f32_e32 v22, 0xbfb8aa3b, v22
	v_mul_f32_e32 v23, 0xbfb8aa3b, v23
	v_exp_f32_e32 v20, v20
	v_exp_f32_e32 v21, v21
	v_exp_f32_e32 v22, v22
	v_exp_f32_e32 v23, v23
	v_mul_f32_e32 v24, 0xbfb8aa3b, v24
	v_mul_f32_e32 v25, 0xbfb8aa3b, v25
	v_exp_f32_e32 v24, v24
	v_exp_f32_e32 v25, v25
	v_add_f32_e32 v18, 1.0, v18
	v_add_f32_e32 v19, 1.0, v19
	v_rcp_f32_e32 v18, v18
	v_rcp_f32_e32 v19, v19
	v_add_f32_e32 v20, 1.0, v20
	v_add_f32_e32 v21, 1.0, v21
	v_add_f32_e32 v22, 1.0, v22
	v_add_f32_e32 v23, 1.0, v23
	v_rcp_f32_e32 v20, v20
	v_rcp_f32_e32 v21, v21
	v_rcp_f32_e32 v22, v22
	v_rcp_f32_e32 v23, v23
	v_add_f32_e32 v24, 1.0, v24
	v_add_f32_e32 v25, 1.0, v25
	v_rcp_f32_e32 v24, v24
	v_rcp_f32_e32 v25, v25
	v_max_f32_e32 v18, 0x35800000, v18
	v_max_f32_e32 v19, 0x35800000, v19
	v_max_f32_e32 v20, 0x35800000, v20
	v_max_f32_e32 v21, 0x35800000, v21
	v_max_f32_e32 v22, 0x35800000, v22
	v_max_f32_e32 v23, 0x35800000, v23
	v_mul_f32_e32 v12, v12, v18
	v_mul_f32_e32 v13, v13, v19
	v_max_f32_e32 v24, 0x35800000, v24
	v_max_f32_e32 v25, 0x35800000, v25
	v_cvt_pk_bf16_f32 v12, v12, v13
	v_mul_f32_e32 v13, v14, v20
	v_mul_f32_e32 v14, v15, v21
	v_mul_f32_e32 v8, v8, v22
	v_mul_f32_e32 v9, v9, v23
	v_lshlrev_b64 v[16:17], 12, v[150:151]
	v_cvt_pk_bf16_f32 v13, v13, v14
	v_cvt_pk_bf16_f32 v14, v8, v9
	v_mul_f32_e32 v8, v10, v24
	v_mul_f32_e32 v9, v11, v25
	v_cvt_pk_bf16_f32 v15, v8, v9
	v_lshl_add_u64 v[8:9], s[16:17], 0, v[16:17]
	v_lshl_add_u64 v[8:9], v[8:9], 0, v[148:149]
	s_waitcnt vmcnt(14)
	v_lshlrev_b32_e32 v10, 16, v204
	v_and_b32_e32 v11, 0xffff0000, v204
	global_store_dwordx4 v[8:9], v[12:15], off
	v_mul_f32_e32 v10, 0xbfb8aa3b, v10
	v_mul_f32_e32 v11, 0xbfb8aa3b, v11
	v_lshlrev_b32_e32 v12, 16, v205
	v_and_b32_e32 v13, 0xffff0000, v205
	v_lshlrev_b32_e32 v14, 16, v206
	v_exp_f32_e32 v10, v10
	v_and_b32_e32 v15, 0xffff0000, v206
	v_exp_f32_e32 v11, v11
	v_mul_f32_e32 v12, 0xbfb8aa3b, v12
	v_mul_f32_e32 v13, 0xbfb8aa3b, v13
	v_lshlrev_b32_e32 v16, 16, v207
	v_exp_f32_e32 v12, v12
	v_exp_f32_e32 v13, v13
	v_mul_f32_e32 v14, 0xbfb8aa3b, v14
	v_mul_f32_e32 v15, 0xbfb8aa3b, v15
	v_and_b32_e32 v17, 0xffff0000, v207
	v_exp_f32_e32 v14, v14
	v_exp_f32_e32 v15, v15
	v_mul_f32_e32 v16, 0xbfb8aa3b, v16
	v_exp_f32_e32 v16, v16
	v_mul_f32_e32 v17, 0xbfb8aa3b, v17
	v_add_f32_e32 v10, 1.0, v10
	v_add_f32_e32 v11, 1.0, v11
	v_exp_f32_e32 v17, v17
	v_rcp_f32_e32 v10, v10
	v_rcp_f32_e32 v11, v11
	v_add_f32_e32 v12, 1.0, v12
	v_add_f32_e32 v13, 1.0, v13
	v_rcp_f32_e32 v12, v12
	v_rcp_f32_e32 v13, v13
	v_add_f32_e32 v14, 1.0, v14
	v_add_f32_e32 v15, 1.0, v15
	v_rcp_f32_e32 v14, v14
	v_rcp_f32_e32 v15, v15
	v_add_f32_e32 v16, 1.0, v16
	v_rcp_f32_e32 v16, v16
	v_add_f32_e32 v17, 1.0, v17
	v_max_f32_e32 v10, 0x35800000, v10
	v_max_f32_e32 v11, 0x35800000, v11
	v_rcp_f32_e32 v17, v17
	v_max_f32_e32 v12, 0x35800000, v12
	v_max_f32_e32 v13, 0x35800000, v13
	v_mul_f32_e32 v0, v0, v10
	v_mul_f32_e32 v1, v1, v11
	v_max_f32_e32 v14, 0x35800000, v14
	v_max_f32_e32 v15, 0x35800000, v15
	v_cvt_pk_bf16_f32 v0, v0, v1
	v_mul_f32_e32 v1, v2, v12
	v_mul_f32_e32 v2, v3, v13
	v_max_f32_e32 v16, 0x35800000, v16
	v_cvt_pk_bf16_f32 v1, v1, v2
	v_mul_f32_e32 v2, v4, v14
	v_mul_f32_e32 v3, v5, v15
	v_max_f32_e32 v17, 0x35800000, v17
	v_cvt_pk_bf16_f32 v2, v2, v3
	v_mul_f32_e32 v3, v6, v16
	v_mul_f32_e32 v4, v7, v17
	v_cvt_pk_bf16_f32 v3, v3, v4
	global_store_dwordx4 v[8:9], v[0:3], off offset:256
	s_cbranch_vccnz .LBB0_860
	s_andn2_b64 vcc, exec, s[6:7]
	v_mov_b64 v[124:125], 0
	v_mov_b64 v[126:127], 0
	v_mov_b64 v[120:121], 0
	v_mov_b64 v[122:123], 0
	v_mov_b64 v[108:109], 0
	v_mov_b64 v[110:111], 0
	v_mov_b64 v[104:105], 0
	v_mov_b64 v[106:107], 0
	v_mov_b64 v[92:93], 0
	v_mov_b64 v[94:95], 0
	v_mov_b64 v[88:89], 0
	v_mov_b64 v[90:91], 0
	v_mov_b64 v[76:77], 0
	v_mov_b64 v[78:79], 0
	v_mov_b64 v[72:73], 0
	v_mov_b64 v[74:75], 0
	v_mov_b64 v[116:117], 0
	v_mov_b64 v[118:119], 0
	v_mov_b64 v[112:113], 0
	v_mov_b64 v[114:115], 0
	v_mov_b64 v[100:101], 0
	v_mov_b64 v[102:103], 0
	v_mov_b64 v[96:97], 0
	v_mov_b64 v[98:99], 0
	v_mov_b64 v[84:85], 0
	v_mov_b64 v[86:87], 0
	v_mov_b64 v[80:81], 0
	v_mov_b64 v[82:83], 0
	v_mov_b64 v[68:69], 0
	v_mov_b64 v[70:71], 0
	v_mov_b64 v[64:65], 0
	v_mov_b64 v[66:67], 0
	v_mov_b64 v[60:61], 0
	v_mov_b64 v[62:63], 0
	v_mov_b64 v[56:57], 0
	v_mov_b64 v[58:59], 0
	v_mov_b64 v[44:45], 0
	v_mov_b64 v[46:47], 0
	v_mov_b64 v[40:41], 0
	v_mov_b64 v[42:43], 0
	v_mov_b64 v[28:29], 0
	v_mov_b64 v[30:31], 0
	v_mov_b64 v[24:25], 0
	v_mov_b64 v[26:27], 0
	v_mov_b64 v[12:13], 0
	v_mov_b64 v[14:15], 0
	v_mov_b64 v[8:9], 0
	v_mov_b64 v[10:11], 0
	v_mov_b64 v[52:53], 0
	v_mov_b64 v[54:55], 0
	v_mov_b64 v[48:49], 0
	v_mov_b64 v[50:51], 0
	v_mov_b64 v[36:37], 0
	v_mov_b64 v[38:39], 0
	v_mov_b64 v[32:33], 0
	v_mov_b64 v[34:35], 0
	v_mov_b64 v[20:21], 0
	v_mov_b64 v[22:23], 0
	v_mov_b64 v[16:17], 0
	v_mov_b64 v[18:19], 0
	v_mov_b64 v[0:1], 0
	v_mov_b64 v[2:3], 0
	v_mov_b64 v[4:5], 0
	v_mov_b64 v[6:7], 0
	s_cbranch_vccnz .LBB0_859
	s_barrier
	s_branch .LBB0_859

.LBB0_1254:
	v_add_u32_e32 v140, 0x10000, v177
	v_add_u32_e32 v141, 0x14000, v177
	ds_read_b128 v[132:135], v140
	ds_read_b128 v[136:139], v140 offset:1024
	ds_read_b128 v[186:189], v140 offset:2048
	ds_read_b128 v[190:193], v140 offset:3072
	ds_read_b128 v[194:197], v141
	ds_read_b128 v[198:201], v141 offset:1024
	ds_read_b128 v[202:205], v141 offset:2048
	ds_read_b128 v[206:209], v141 offset:3072
	s_add_i32 s10, s6, s5
	s_add_i32 s11, s5, 0xffffff80
	s_cmp_eq_u32 s4, 12
	s_cselect_b64 vcc, -1, 0
	s_and_b64 s[8:9], vcc, exec
	v_cndmask_b32_e32 v140, v128, v182, vcc
	s_cselect_b32 s7, 0, s5
	v_cndmask_b32_e32 v141, v130, v184, vcc
	v_cndmask_b32_e32 v142, v129, v183, vcc
	s_mov_b32 m0, s57
	ds_read_b128 v[210:213], v178
	ds_read_b128 v[214:217], v178 offset:1024
	ds_read_b128 v[218:221], v178 offset:2048
	ds_read_b128 v[222:225], v178 offset:3072
	ds_read_b128 v[226:229], v178 offset:4096
	ds_read_b128 v[230:233], v178 offset:5120
	ds_read_b128 v[234:237], v178 offset:6144
	ds_read_b128 v[238:241], v178 offset:7168
	buffer_load_dwordx4 v130, s[20:23], s11 offen lds
	s_mov_b32 m0, s58
	s_cselect_b32 s8, s80, s10
	buffer_load_dwordx4 v131, s[20:23], s11 offen lds
	s_waitcnt vmcnt(8)
	s_waitcnt lgkmcnt(0)
	s_barrier
	s_setprio 1
	s_nop 1
	s_waitcnt lgkmcnt(6)
	v_mfma_f32_16x16x128_f8f6f4 v[124:127], v[132:139], v[210:217], v[124:127]
	v_mfma_f32_16x16x128_f8f6f4 v[120:123], v[186:193], v[210:217], v[120:123]
	s_waitcnt lgkmcnt(4)
	v_mfma_f32_16x16x128_f8f6f4 v[108:111], v[132:139], v[218:225], v[108:111]
	v_mfma_f32_16x16x128_f8f6f4 v[104:107], v[186:193], v[218:225], v[104:107]
	s_waitcnt lgkmcnt(2)
	v_mfma_f32_16x16x128_f8f6f4 v[92:95], v[132:139], v[226:233], v[92:95]
	v_mfma_f32_16x16x128_f8f6f4 v[88:91], v[186:193], v[226:233], v[88:91]
	s_waitcnt lgkmcnt(0)
	v_mfma_f32_16x16x128_f8f6f4 v[76:79], v[132:139], v[234:241], v[76:79]
	v_mfma_f32_16x16x128_f8f6f4 v[72:75], v[186:193], v[234:241], v[72:75]
	s_setprio 0
	s_setprio 1
	s_nop 1
	v_mfma_f32_16x16x128_f8f6f4 v[116:119], v[194:201], v[210:217], v[116:119]
	v_mfma_f32_16x16x128_f8f6f4 v[112:115], v[202:209], v[210:217], v[112:115]
	v_mfma_f32_16x16x128_f8f6f4 v[100:103], v[194:201], v[218:225], v[100:103]
	v_mfma_f32_16x16x128_f8f6f4 v[96:99], v[202:209], v[218:225], v[96:99]
	v_mfma_f32_16x16x128_f8f6f4 v[84:87], v[194:201], v[226:233], v[84:87]
	v_mfma_f32_16x16x128_f8f6f4 v[80:83], v[202:209], v[226:233], v[80:83]
	v_mfma_f32_16x16x128_f8f6f4 v[68:71], v[194:201], v[234:241], v[68:71]
	v_mfma_f32_16x16x128_f8f6f4 v[64:67], v[202:209], v[234:241], v[64:67]
	s_setprio 0
	s_barrier
	s_mov_b32 m0, s43
	s_mov_b32 s26, s22
	s_mov_b32 s27, s23
	ds_read_b128 v[210:213], v178 offset:16384
	ds_read_b128 v[214:217], v178 offset:17408
	ds_read_b128 v[218:221], v178 offset:18432
	ds_read_b128 v[222:225], v178 offset:19456
	ds_read_b128 v[226:229], v178 offset:20480
	ds_read_b128 v[230:233], v178 offset:21504
	ds_read_b128 v[234:237], v178 offset:22528
	ds_read_b128 v[238:241], v178 offset:23552
	buffer_load_dwordx4 v155, s[24:27], s8 offen lds
	s_mov_b32 m0, s44
	s_add_i32 s9, s8, 0x4000
	buffer_load_dwordx4 v161, s[24:27], s8 offen lds
	s_mov_b32 m0, s45
	s_nop 0
	buffer_load_dwordx4 v155, s[24:27], s9 offen lds
	s_mov_b32 m0, s46
	s_nop 0
	buffer_load_dwordx4 v161, s[24:27], s9 offen lds
	s_mov_b32 m0, s42
	s_nop 0
	buffer_load_dwordx4 v140, s[20:23], s7 offen lds
	s_mov_b32 m0, s47
	s_nop 0
	buffer_load_dwordx4 v142, s[20:23], s7 offen lds
	s_waitcnt vmcnt(8)
	s_waitcnt lgkmcnt(0)
	s_barrier
	s_setprio 1
	s_nop 1
	s_waitcnt lgkmcnt(6)
	v_mfma_f32_16x16x128_f8f6f4 v[60:63], v[132:139], v[210:217], v[60:63]
	v_mfma_f32_16x16x128_f8f6f4 v[56:59], v[186:193], v[210:217], v[56:59]
	s_waitcnt lgkmcnt(4)
	v_mfma_f32_16x16x128_f8f6f4 v[44:47], v[132:139], v[218:225], v[44:47]
	v_mfma_f32_16x16x128_f8f6f4 v[40:43], v[186:193], v[218:225], v[40:43]
	s_waitcnt lgkmcnt(2)
	v_mfma_f32_16x16x128_f8f6f4 v[28:31], v[132:139], v[226:233], v[28:31]
	v_mfma_f32_16x16x128_f8f6f4 v[24:27], v[186:193], v[226:233], v[24:27]
	s_waitcnt lgkmcnt(0)
	v_mfma_f32_16x16x128_f8f6f4 v[12:15], v[132:139], v[234:241], v[12:15]
	v_mfma_f32_16x16x128_f8f6f4 v[8:11], v[186:193], v[234:241], v[8:11]
	s_setprio 0
	s_setprio 1
	s_nop 1
	v_mfma_f32_16x16x128_f8f6f4 v[52:55], v[194:201], v[210:217], v[52:55]
	v_mfma_f32_16x16x128_f8f6f4 v[48:51], v[202:209], v[210:217], v[48:51]
	v_mfma_f32_16x16x128_f8f6f4 v[36:39], v[194:201], v[218:225], v[36:39]
	v_mfma_f32_16x16x128_f8f6f4 v[32:35], v[202:209], v[218:225], v[32:35]
	v_mfma_f32_16x16x128_f8f6f4 v[20:23], v[194:201], v[226:233], v[20:23]
	v_mfma_f32_16x16x128_f8f6f4 v[16:19], v[202:209], v[226:233], v[16:19]
	v_mfma_f32_16x16x128_f8f6f4 v[4:7], v[194:201], v[234:241], v[4:7]
	v_mfma_f32_16x16x128_f8f6f4 v[0:3], v[202:209], v[234:241], v[0:3]
	s_setprio 0
	s_barrier
	v_add_u32_e32 v143, 0x18000, v177
	ds_read_b128 v[132:135], v143
	ds_read_b128 v[136:139], v143 offset:1024
	ds_read_b128 v[186:189], v143 offset:2048
	ds_read_b128 v[190:193], v143 offset:3072
	v_add_u32_e32 v143, 0x1c000, v177
	ds_read_b128 v[194:197], v143
	ds_read_b128 v[198:201], v143 offset:1024
	ds_read_b128 v[202:205], v143 offset:2048
	ds_read_b128 v[206:209], v143 offset:3072
	s_mov_b32 m0, s48
	ds_read_b128 v[210:213], v178 offset:32768
	ds_read_b128 v[214:217], v178 offset:33792
	ds_read_b128 v[218:221], v178 offset:34816
	ds_read_b128 v[222:225], v178 offset:35840
	ds_read_b128 v[226:229], v178 offset:36864
	ds_read_b128 v[230:233], v178 offset:37888
	ds_read_b128 v[234:237], v178 offset:38912
	ds_read_b128 v[238:241], v178 offset:39936
	v_cndmask_b32_e32 v143, v131, v185, vcc
	buffer_load_dwordx4 v141, s[20:23], s7 offen lds
	s_mov_b32 m0, s49
	s_nop 0
	buffer_load_dwordx4 v143, s[20:23], s7 offen lds
	s_waitcnt vmcnt(8)
	s_waitcnt lgkmcnt(0)
	s_barrier
	s_setprio 1
	s_nop 1
	s_waitcnt lgkmcnt(6)
	v_mfma_f32_16x16x128_f8f6f4 v[124:127], v[132:139], v[210:217], v[124:127]
	v_mfma_f32_16x16x128_f8f6f4 v[120:123], v[186:193], v[210:217], v[120:123]
	s_waitcnt lgkmcnt(4)
	v_mfma_f32_16x16x128_f8f6f4 v[108:111], v[132:139], v[218:225], v[108:111]
	v_mfma_f32_16x16x128_f8f6f4 v[104:107], v[186:193], v[218:225], v[104:107]
	s_waitcnt lgkmcnt(2)
	v_mfma_f32_16x16x128_f8f6f4 v[92:95], v[132:139], v[226:233], v[92:95]
	v_mfma_f32_16x16x128_f8f6f4 v[88:91], v[186:193], v[226:233], v[88:91]
	s_waitcnt lgkmcnt(0)
	v_mfma_f32_16x16x128_f8f6f4 v[76:79], v[132:139], v[234:241], v[76:79]
	v_mfma_f32_16x16x128_f8f6f4 v[72:75], v[186:193], v[234:241], v[72:75]
	s_setprio 0
	s_setprio 1
	s_nop 1
	v_mfma_f32_16x16x128_f8f6f4 v[116:119], v[194:201], v[210:217], v[116:119]
	v_mfma_f32_16x16x128_f8f6f4 v[112:115], v[202:209], v[210:217], v[112:115]
	v_mfma_f32_16x16x128_f8f6f4 v[100:103], v[194:201], v[218:225], v[100:103]
	v_mfma_f32_16x16x128_f8f6f4 v[96:99], v[202:209], v[218:225], v[96:99]
	v_mfma_f32_16x16x128_f8f6f4 v[84:87], v[194:201], v[226:233], v[84:87]
	v_mfma_f32_16x16x128_f8f6f4 v[80:83], v[202:209], v[226:233], v[80:83]
	v_mfma_f32_16x16x128_f8f6f4 v[68:71], v[194:201], v[234:241], v[68:71]
	v_mfma_f32_16x16x128_f8f6f4 v[64:67], v[202:209], v[234:241], v[64:67]
	s_setprio 0
	s_barrier
	s_mov_b32 m0, s51
	s_add_i32 s9, s8, 0x80
	ds_read_b128 v[210:213], v178 offset:49152
	ds_read_b128 v[214:217], v178 offset:50176
	ds_read_b128 v[218:221], v178 offset:51200
	ds_read_b128 v[222:225], v178 offset:52224
	ds_read_b128 v[226:229], v178 offset:53248
	ds_read_b128 v[230:233], v178 offset:54272
	ds_read_b128 v[234:237], v178 offset:55296
	ds_read_b128 v[238:241], v178 offset:56320
	buffer_load_dwordx4 v155, s[24:27], s9 offen lds
	s_mov_b32 m0, s52
	s_add_i32 s8, s8, 0x4080
	buffer_load_dwordx4 v161, s[24:27], s9 offen lds
	s_mov_b32 m0, s55
	s_bitset1_b32 s7, 7
	buffer_load_dwordx4 v155, s[24:27], s8 offen lds
	s_mov_b32 m0, s56
	s_nop 0
	buffer_load_dwordx4 v161, s[24:27], s8 offen lds
	s_mov_b32 m0, s53
	s_nop 0
	buffer_load_dwordx4 v140, s[20:23], s7 offen lds
	s_mov_b32 m0, s54
	s_nop 0
	buffer_load_dwordx4 v142, s[20:23], s7 offen lds
	s_waitcnt vmcnt(8)
	s_waitcnt lgkmcnt(0)
	s_barrier
	s_setprio 1
	s_nop 1
	s_waitcnt lgkmcnt(6)
	v_mfma_f32_16x16x128_f8f6f4 v[60:63], v[132:139], v[210:217], v[60:63]
	v_mfma_f32_16x16x128_f8f6f4 v[56:59], v[186:193], v[210:217], v[56:59]
	s_waitcnt lgkmcnt(4)
	v_mfma_f32_16x16x128_f8f6f4 v[44:47], v[132:139], v[218:225], v[44:47]
	v_mfma_f32_16x16x128_f8f6f4 v[40:43], v[186:193], v[218:225], v[40:43]
	s_waitcnt lgkmcnt(2)
	v_mfma_f32_16x16x128_f8f6f4 v[28:31], v[132:139], v[226:233], v[28:31]
	v_mfma_f32_16x16x128_f8f6f4 v[24:27], v[186:193], v[226:233], v[24:27]
	s_waitcnt lgkmcnt(0)
	v_mfma_f32_16x16x128_f8f6f4 v[12:15], v[132:139], v[234:241], v[12:15]
	v_mfma_f32_16x16x128_f8f6f4 v[8:11], v[186:193], v[234:241], v[8:11]
	s_setprio 0
	s_setprio 1
	s_nop 1
	v_mfma_f32_16x16x128_f8f6f4 v[52:55], v[194:201], v[210:217], v[52:55]
	v_mfma_f32_16x16x128_f8f6f4 v[48:51], v[202:209], v[210:217], v[48:51]
	v_mfma_f32_16x16x128_f8f6f4 v[36:39], v[194:201], v[218:225], v[36:39]
	v_mfma_f32_16x16x128_f8f6f4 v[32:35], v[202:209], v[218:225], v[32:35]
	v_mfma_f32_16x16x128_f8f6f4 v[20:23], v[194:201], v[226:233], v[20:23]
	v_mfma_f32_16x16x128_f8f6f4 v[16:19], v[202:209], v[226:233], v[16:19]
	v_mfma_f32_16x16x128_f8f6f4 v[4:7], v[194:201], v[234:241], v[4:7]
	v_mfma_f32_16x16x128_f8f6f4 v[0:3], v[202:209], v[234:241], v[0:3]
	s_setprio 0
	s_barrier
	s_add_i32 s4, s4, 2
	s_addk_i32 s5, 0x100
	s_cmp_gt_u32 s4, 13
	s_cbranch_scc0 .LBB0_1254
	v_ashrrev_i32_e32 v147, 31, v146
	v_readlane_b32 s4, v253, 45
	v_lshlrev_b64 v[128:129], 13, v[146:147]
	v_readlane_b32 s16, v253, 57
	v_readlane_b32 s17, v253, 58
	v_readlane_b32 s14, v253, 55
	v_readlane_b32 s15, v253, 56
	v_lshl_add_u64 v[128:129], s[16:17], 0, v[128:129]
	v_cmp_gt_i32_e64 s[16:17], s81, v168
	v_readlane_b32 s12, v253, 53
	v_readlane_b32 s13, v253, 54
	v_cndmask_b32_e64 v144, 0, v168, s[16:17]
	v_cmp_gt_i32_e64 s[14:15], s81, v170
	v_readlane_b32 s10, v253, 51
	v_readlane_b32 s11, v253, 52
	v_lshlrev_b32_e32 v163, 2, v144
	v_cndmask_b32_e64 v144, 0, v170, s[14:15]
	v_cmp_gt_i32_e64 s[12:13], s81, v171
	v_readlane_b32 s8, v253, 49
	v_readlane_b32 s9, v253, 50
	v_lshlrev_b32_e32 v150, 2, v144
	v_cndmask_b32_e64 v144, 0, v171, s[12:13]
	v_cmp_gt_i32_e64 s[10:11], s81, v172
	v_lshl_or_b32 v148, s1, 8, v169
	s_ashr_i32 s1, s0, 31
	v_lshlrev_b64 v[164:165], 18, v[146:147]
	v_lshlrev_b32_e32 v152, 2, v144
	v_cndmask_b32_e64 v144, 0, v172, s[10:11]
	v_cmp_gt_i32_e64 s[8:9], s81, v173
	v_lshl_add_u64 v[146:147], s[34:35], 0, v[164:165]
	s_lshl_b64 s[0:1], s[0:1], 2
	v_lshlrev_b32_e32 v154, 2, v144
	v_cndmask_b32_e64 v144, 0, v173, s[8:9]
	v_readlane_b32 s5, v253, 46
	v_readlane_b32 s6, v253, 47
	v_readlane_b32 s7, v253, 48
	v_ashrrev_i32_e32 v149, 31, v148
	v_lshl_add_u64 v[146:147], v[146:147], 0, s[0:1]
	v_lshlrev_b64 v[192:193], 2, v[144:145]
	s_nop 15
	s_nop 15
	v_lshl_add_u64 v[132:133], v[148:149], 2, v[128:129]
	v_readfirstlane_b32 s4, v146
	v_readfirstlane_b32 s5, v147
	v_lshl_add_u64 v[186:187], v[146:147], 0, v[192:193]
	v_cmp_gt_i32_e64 s[6:7], s81, v174
	global_load_dwordx4 v[136:139], v[132:133], off offset:16
	global_load_dwordx4 v[140:143], v[132:133], off
	global_load_dwordx4 v[128:131], v[132:133], off offset:48
	s_nop 0
	global_load_dwordx4 v[132:135], v[132:133], off offset:32
	v_cndmask_b32_e64 v144, 0, v174, s[6:7]
	global_load_dword v162, v163, s[4:5]
	global_load_dword v191, v150, s[4:5]
	global_load_dword v190, v152, s[4:5]
	global_load_dword v188, v[186:187], off
	global_load_dword v189, v154, s[4:5]
	v_cmp_gt_i32_e64 s[4:5], s81, v175
	v_lshlrev_b64 v[194:195], 2, v[144:145]
	v_cmp_gt_i32_e32 vcc, s81, v176
	v_cndmask_b32_e64 v144, 0, v175, s[4:5]
	v_lshlrev_b64 v[196:197], 2, v[144:145]
	v_lshl_add_u64 v[186:187], v[146:147], 0, v[194:195]
	v_lshl_add_u64 v[198:199], v[146:147], 0, v[196:197]
	v_cndmask_b32_e32 v144, 0, v176, vcc
	v_lshl_add_u64 v[164:165], s[30:31], 0, v[164:165]
	global_load_dword v187, v[186:187], off
	v_lshl_add_u64 v[164:165], v[164:165], 0, s[0:1]
	global_load_dword v186, v[198:199], off
	v_lshlrev_b64 v[198:199], 2, v[144:145]
	v_lshl_add_u64 v[146:147], v[146:147], 0, v[198:199]
	v_readfirstlane_b32 s0, v164
	v_readfirstlane_b32 s1, v165
	v_lshl_add_u64 v[192:193], v[164:165], 0, v[192:193]
	global_load_dword v147, v[146:147], off
	s_nop 2
	global_load_dword v160, v150, s[0:1]
	global_load_dword v158, v152, s[0:1]
	global_load_dword v156, v154, s[0:1]
	v_readlane_b32 s18, v253, 59
	global_load_dword v154, v[192:193], off
	v_lshl_add_u64 v[192:193], v[164:165], 0, v[194:195]
	global_load_dword v152, v[192:193], off
	v_lshl_add_u64 v[192:193], v[164:165], 0, v[196:197]
	global_load_dword v150, v[192:193], off
	v_lshl_add_u64 v[192:193], v[164:165], 0, v[198:199]
	global_load_dword v146, v[192:193], off
	global_load_dword v242, v163, s[0:1]
	s_cmp_lg_u64 s[38:39], 0
	s_cbranch_scc0 .LBB0_1257
	s_barrier
.LBB0_1257:
	v_readlane_b32 s19, v253, 60
	s_waitcnt vmcnt(0)
	v_cndmask_b32_e64 v162, -1, v162, s[16:17]
	v_cmp_lt_i32_e64 s[0:1], -1, v162
	s_and_saveexec_b64 s[16:17], s[0:1]
	s_cbranch_execz .LBB0_1259
	v_mul_f32_e32 v242, 0x41800000, v242
	v_pk_fma_f32 v[124:125], v[124:125], s[40:41], v[140:141] op_sel_hi:[1,0,1]
	v_pk_fma_f32 v[120:121], v[120:121], s[40:41], v[136:137] op_sel_hi:[1,0,1]
	v_pk_fma_f32 v[116:117], v[116:117], s[40:41], v[132:133] op_sel_hi:[1,0,1]
	v_pk_fma_f32 v[112:113], v[112:113], s[40:41], v[128:129] op_sel_hi:[1,0,1]
	v_pk_fma_f32 v[126:127], v[126:127], s[40:41], v[142:143] op_sel_hi:[1,0,1]
	v_pk_fma_f32 v[122:123], v[122:123], s[40:41], v[138:139] op_sel_hi:[1,0,1]
	v_pk_fma_f32 v[118:119], v[118:119], s[40:41], v[134:135] op_sel_hi:[1,0,1]
	v_pk_fma_f32 v[114:115], v[114:115], s[40:41], v[130:131] op_sel_hi:[1,0,1]
	v_mov_b32_e32 v163, v145
	v_lshlrev_b64 v[162:163], 11, v[162:163]
	v_pk_mul_f32 v[124:125], v[124:125], v[242:243] op_sel_hi:[1,0]
	v_pk_mul_f32 v[120:121], v[120:121], v[242:243] op_sel_hi:[1,0]
	v_pk_mul_f32 v[116:117], v[116:117], v[242:243] op_sel_hi:[1,0]
	v_pk_mul_f32 v[112:113], v[112:113], v[242:243] op_sel_hi:[1,0]
	v_med3_f32 v124, v124, s75, v180
	v_med3_f32 v125, v125, s75, v180
	v_med3_f32 v120, v120, s75, v180
	v_med3_f32 v121, v121, s75, v180
	v_med3_f32 v116, v116, s75, v180
	v_med3_f32 v117, v117, s75, v180
	v_med3_f32 v112, v112, s75, v180
	v_med3_f32 v113, v113, s75, v180
	v_cvt_pk_fp8_f32 v200, v124, v125
	v_cvt_pk_fp8_f32 v201, v120, v121
	v_pk_mul_f32 v[126:127], v[126:127], v[242:243] op_sel_hi:[1,0]
	v_pk_mul_f32 v[122:123], v[122:123], v[242:243] op_sel_hi:[1,0]
	v_cvt_pk_fp8_f32 v202, v116, v117
	v_cvt_pk_fp8_f32 v203, v112, v113
	v_pk_mul_f32 v[118:119], v[118:119], v[242:243] op_sel_hi:[1,0]
	v_pk_mul_f32 v[114:115], v[114:115], v[242:243] op_sel_hi:[1,0]
	v_med3_f32 v126, v126, s75, v180
	v_med3_f32 v127, v127, s75, v180
	v_med3_f32 v122, v122, s75, v180
	v_med3_f32 v123, v123, s75, v180
	v_med3_f32 v118, v118, s75, v180
	v_med3_f32 v119, v119, s75, v180
	v_med3_f32 v114, v114, s75, v180
	v_med3_f32 v115, v115, s75, v180
	v_cvt_pk_fp8_f32 v200, v126, v127 op_sel:[0,0,1]
	v_cvt_pk_fp8_f32 v201, v122, v123 op_sel:[0,0,1]
	v_cvt_pk_fp8_f32 v202, v118, v119 op_sel:[0,0,1]
	v_cvt_pk_fp8_f32 v203, v114, v115 op_sel:[0,0,1]
	v_lshl_add_u64 v[112:113], s[36:37], 0, v[162:163]
	v_lshl_add_u64 v[112:113], v[112:113], 0, v[148:149]
	global_store_dwordx4 v[112:113], v[200:203], off
